# lean gate/up weight conversion (no per-column address math) in P2 loop and in the c1 task loop
# speedup vs baseline: 1.0561x; 1.0016x over previous
.Llean_entry:
	v_mov_b32_e32 v194, 0x23f70
	v_mov_b32_e32 v196, 0x23f78
	ds_read_b64 v[194:195], v194
	ds_read_b64 v[196:197], v196
	s_waitcnt lgkmcnt(0)
	v_readfirstlane_b32 s38, v194
	v_readfirstlane_b32 s39, v195
	v_readfirstlane_b32 s40, v196
	v_readfirstlane_b32 s41, v197
	s_nop 3
	v_and_b32_e32 v194, 63, v0
	v_lshrrev_b32_e32 v195, 6, v0
	v_lshrrev_b32_e32 v188, 3, v194
	v_lshlrev_b32_e32 v188, 14, v188
	v_lshl_add_u32 v188, v195, 7, v188
	v_and_b32_e32 v189, 7, v194
	v_lshl_add_u32 v188, v189, 4, v188
	v_lshrrev_b32_e32 v192, 2, v195
	v_lshlrev_b32_e32 v192, 18, v192
	v_and_b32_e32 v190, 3, v195
	v_lshl_add_u32 v192, v190, 12, v192
	v_lshl_add_u32 v192, v189, 9, v192
	v_lshrrev_b32_e32 v190, 3, v194
	v_lshl_add_u32 v192, v190, 4, v192
	v_add_u32_e32 v189, 0x1000, v188
	v_add_u32_e32 v190, 0x2000, v188
	v_add_u32_e32 v191, 0x3000, v188
	s_mov_b32 s70, 0x42000000
	s_mov_b32 s71, 0x42000000
.Llean_top:
	s_cmp_gt_i32 s27, s56
	s_cbranch_scc1 .LBB0_238
	s_and_b32 s37, s27, 0x7ff
	s_lshr_b32 s44, s37, 3
	s_and_b32 s37, s37, 7
	s_lshr_b32 s65, s27, 11
	s_lshl_b32 s50, s44, 19
	s_lshl_b32 s51, s37, 15
	s_add_i32 s50, s50, s51
	s_lshl_b32 s51, s65, 14
	s_add_i32 s50, s50, s51
	s_add_u32 s50, s50, 0x94c000
	s_add_u32 s50, s50, s42
	s_addc_u32 s51, s43, 0
	s_cmp_eq_u32 s65, 0
	s_cselect_b32 s48, s38, s40
	s_cselect_b32 s49, s39, s41
	s_lshl_b32 s44, s44, 20
	s_lshl_b32 s37, s37, 17
	s_add_i32 s44, s44, s37
	s_add_i32 s44, s44, s23
	s_add_u32 s48, s48, s44
	s_addc_u32 s49, s49, 0
	global_load_dwordx4 v[108:111], v188, s[48:49] nt
	global_load_dwordx4 v[112:115], v188, s[48:49] offset:1024 nt
	global_load_dwordx4 v[116:119], v188, s[48:49] offset:2048 nt
	global_load_dwordx4 v[120:123], v188, s[48:49] offset:3072 nt
	global_load_dwordx4 v[124:127], v189, s[48:49] nt
	global_load_dwordx4 v[128:131], v189, s[48:49] offset:1024 nt
	global_load_dwordx4 v[132:135], v189, s[48:49] offset:2048 nt
	global_load_dwordx4 v[136:139], v189, s[48:49] offset:3072 nt
	global_load_dwordx4 v[140:143], v190, s[48:49] nt
	global_load_dwordx4 v[144:147], v190, s[48:49] offset:1024 nt
	global_load_dwordx4 v[148:151], v190, s[48:49] offset:2048 nt
	global_load_dwordx4 v[152:155], v190, s[48:49] offset:3072 nt
	global_load_dwordx4 v[156:159], v191, s[48:49] nt
	global_load_dwordx4 v[160:163], v191, s[48:49] offset:1024 nt
	global_load_dwordx4 v[164:167], v191, s[48:49] offset:2048 nt
	global_load_dwordx4 v[168:171], v191, s[48:49] offset:3072 nt
	s_waitcnt vmcnt(0)
	v_pk_mul_f32 v[108:109], v[108:109], s[70:71] op_sel_hi:[1,0]
	v_pk_mul_f32 v[110:111], v[110:111], s[70:71] op_sel_hi:[1,0]
	v_pk_mul_f32 v[112:113], v[112:113], s[70:71] op_sel_hi:[1,0]
	v_pk_mul_f32 v[114:115], v[114:115], s[70:71] op_sel_hi:[1,0]
	v_pk_mul_f32 v[116:117], v[116:117], s[70:71] op_sel_hi:[1,0]
	v_pk_mul_f32 v[118:119], v[118:119], s[70:71] op_sel_hi:[1,0]
	v_pk_mul_f32 v[120:121], v[120:121], s[70:71] op_sel_hi:[1,0]
	v_pk_mul_f32 v[122:123], v[122:123], s[70:71] op_sel_hi:[1,0]
	v_pk_mul_f32 v[124:125], v[124:125], s[70:71] op_sel_hi:[1,0]
	v_pk_mul_f32 v[126:127], v[126:127], s[70:71] op_sel_hi:[1,0]
	v_pk_mul_f32 v[128:129], v[128:129], s[70:71] op_sel_hi:[1,0]
	v_pk_mul_f32 v[130:131], v[130:131], s[70:71] op_sel_hi:[1,0]
	v_pk_mul_f32 v[132:133], v[132:133], s[70:71] op_sel_hi:[1,0]
	v_pk_mul_f32 v[134:135], v[134:135], s[70:71] op_sel_hi:[1,0]
	v_pk_mul_f32 v[136:137], v[136:137], s[70:71] op_sel_hi:[1,0]
	v_pk_mul_f32 v[138:139], v[138:139], s[70:71] op_sel_hi:[1,0]
	v_pk_mul_f32 v[140:141], v[140:141], s[70:71] op_sel_hi:[1,0]
	v_pk_mul_f32 v[142:143], v[142:143], s[70:71] op_sel_hi:[1,0]
	v_pk_mul_f32 v[144:145], v[144:145], s[70:71] op_sel_hi:[1,0]
	v_pk_mul_f32 v[146:147], v[146:147], s[70:71] op_sel_hi:[1,0]
	v_pk_mul_f32 v[148:149], v[148:149], s[70:71] op_sel_hi:[1,0]
	v_pk_mul_f32 v[150:151], v[150:151], s[70:71] op_sel_hi:[1,0]
	v_pk_mul_f32 v[152:153], v[152:153], s[70:71] op_sel_hi:[1,0]
	v_pk_mul_f32 v[154:155], v[154:155], s[70:71] op_sel_hi:[1,0]
	v_pk_mul_f32 v[156:157], v[156:157], s[70:71] op_sel_hi:[1,0]
	v_pk_mul_f32 v[158:159], v[158:159], s[70:71] op_sel_hi:[1,0]
	v_pk_mul_f32 v[160:161], v[160:161], s[70:71] op_sel_hi:[1,0]
	v_pk_mul_f32 v[162:163], v[162:163], s[70:71] op_sel_hi:[1,0]
	v_pk_mul_f32 v[164:165], v[164:165], s[70:71] op_sel_hi:[1,0]
	v_pk_mul_f32 v[166:167], v[166:167], s[70:71] op_sel_hi:[1,0]
	v_pk_mul_f32 v[168:169], v[168:169], s[70:71] op_sel_hi:[1,0]
	v_pk_mul_f32 v[170:171], v[170:171], s[70:71] op_sel_hi:[1,0]
	v_cvt_pk_fp8_f32 v172, v108, v112
	v_cvt_pk_fp8_f32 v173, v124, v128
	v_cvt_pk_fp8_f32 v174, v140, v144
	v_cvt_pk_fp8_f32 v175, v156, v160
	v_cvt_pk_fp8_f32 v176, v109, v113
	v_cvt_pk_fp8_f32 v177, v125, v129
	v_cvt_pk_fp8_f32 v178, v141, v145
	v_cvt_pk_fp8_f32 v179, v157, v161
	v_cvt_pk_fp8_f32 v180, v110, v114
	v_cvt_pk_fp8_f32 v181, v126, v130
	v_cvt_pk_fp8_f32 v182, v142, v146
	v_cvt_pk_fp8_f32 v183, v158, v162
	v_cvt_pk_fp8_f32 v184, v111, v115
	v_cvt_pk_fp8_f32 v185, v127, v131
	v_cvt_pk_fp8_f32 v186, v143, v147
	v_cvt_pk_fp8_f32 v187, v159, v163
	v_cvt_pk_fp8_f32 v172, v116, v120 op_sel:[0,0,1]
	v_cvt_pk_fp8_f32 v173, v132, v136 op_sel:[0,0,1]
	v_cvt_pk_fp8_f32 v174, v148, v152 op_sel:[0,0,1]
	v_cvt_pk_fp8_f32 v175, v164, v168 op_sel:[0,0,1]
	v_cvt_pk_fp8_f32 v176, v117, v121 op_sel:[0,0,1]
	v_cvt_pk_fp8_f32 v177, v133, v137 op_sel:[0,0,1]
	v_cvt_pk_fp8_f32 v178, v149, v153 op_sel:[0,0,1]
	v_cvt_pk_fp8_f32 v179, v165, v169 op_sel:[0,0,1]
	v_cvt_pk_fp8_f32 v180, v118, v122 op_sel:[0,0,1]
	v_cvt_pk_fp8_f32 v181, v134, v138 op_sel:[0,0,1]
	v_cvt_pk_fp8_f32 v182, v150, v154 op_sel:[0,0,1]
	v_cvt_pk_fp8_f32 v183, v166, v170 op_sel:[0,0,1]
	v_cvt_pk_fp8_f32 v184, v119, v123 op_sel:[0,0,1]
	v_cvt_pk_fp8_f32 v185, v135, v139 op_sel:[0,0,1]
	v_cvt_pk_fp8_f32 v186, v151, v155 op_sel:[0,0,1]
	v_cvt_pk_fp8_f32 v187, v167, v171 op_sel:[0,0,1]
	global_store_dwordx4 v192, v[172:175], s[50:51]
	global_store_dwordx4 v192, v[176:179], s[50:51] offset:128
	global_store_dwordx4 v192, v[180:183], s[50:51] offset:256
	global_store_dwordx4 v192, v[184:187], s[50:51] offset:384
	s_add_i32 s25, s25, -1
	s_add_i32 s27, s27, s18
	s_cmp_lg_u32 s25, 0
	s_cbranch_scc1 .Llean_top
	s_branch .LBB0_238

.LBB0_496:
	v_bfe_u32 v48, v20, 2, 6
	v_lshlrev_b32_e32 v19, 3, v14
	v_lshlrev_b32_e32 v14, s3, v48
	v_add_u32_e32 v16, s2, v14
	v_mov_b64_e32 v[14:15], s[16:17]
	v_mad_i64_i32 v[14:15], s[2:3], v16, s33, v[14:15]
	v_and_b32_e32 v68, 48, v22
	v_lshl_add_u64 v[14:15], v[14:15], 0, v[68:69]
	global_load_dwordx4 v[14:17], v[14:15], off offset:1536
	s_add_u32 s0, s18, 0x4e872100
	s_addc_u32 s1, s19, 0
	v_and_b32_e32 v22, 0x70, v22
	s_movk_i32 s10, 0x90
	s_add_i32 s2, 0, 0x1b000
	v_lshl_add_u32 v38, v47, 1, 0
	v_add_u32_e32 v37, s2, v22
	v_mul_u32_u24_e32 v39, 0x90, v22
	v_mad_u32_u24 v49, v22, s10, v38
	v_lshlrev_b32_e32 v22, 5, v20
	v_lshrrev_b32_e32 v23, 2, v20
	v_and_b32_e32 v24, 64, v22
	v_add_u32_e32 v23, v24, v23
	s_movk_i32 s4, 0x44
	v_mul_lo_u32 v23, v23, s4
	v_and_b32_e32 v22, 32, v22
	s_lshl_b32 s8, s20, 3
	v_add3_u32 v50, 0, v23, v22
	s_lshl_b32 s4, s20, 5
	v_mul_u32_u24_e32 v22, 0x48, v21
	s_ashr_i32 s9, s8, 31
	s_add_i32 s31, s4, 0
	s_ashr_i32 s21, s20, 31
	v_add_lshl_u32 v41, s8, v22, 1
	s_lshl_b64 s[8:9], s[8:9], 2
	s_add_u32 s7, s18, s8
	s_addc_u32 s8, s19, s9
	s_add_u32 s34, s7, 0x56c72100
	s_addc_u32 s35, s8, 0
	s_cmp_gt_u32 s30, 1
	s_cselect_b64 s[22:23], -1, 0
	s_and_b64 s[8:9], s[22:23], exec
	v_lshrrev_b32_e32 v22, 4, v21
	s_cselect_b32 s37, 6, 0
	s_bfe_u32 s6, s6, 0x10006
	v_and_b32_e32 v24, 15, v20
	v_lshlrev_b32_e32 v25, 3, v22
	v_lshlrev_b32_e32 v22, 2, v22
	v_lshl_or_b32 v29, s6, 6, v24
	v_lshl_or_b32 v30, s6, 7, v22
	s_lshl_b64 s[6:7], s[20:21], 10
	s_add_u32 s6, s18, s6
	v_lshlrev_b32_e32 v22, 4, v21
	v_mov_b32_e32 v23, v69
	s_addc_u32 s7, s19, s7
	v_lshl_add_u64 v[22:23], s[6:7], 0, v[22:23]
	s_mov_b64 s[6:7], 0x5f17a100
	v_lshl_add_u64 v[26:27], v[22:23], 0, s[6:7]
	s_lshl_b32 s6, s20, 4
	s_and_b32 s7, s6, 0xffffffe0
	v_mul_u32_u24_e32 v40, 0x44, v21
	v_lshl_add_u32 v42, v21, 1, 0
	v_cmp_eq_u32_e64 s[4:5], 0, v21
	v_or_b32_e32 v21, s7, v24
	s_movk_i32 s21, 0x48
	v_or_b32_e32 v28, 32, v25
	v_mul_lo_u32 v21, v21, s21
	v_add_lshl_u32 v44, v21, v25, 1
	v_add_lshl_u32 v45, v21, v28, 1
	v_add_u32_e32 v21, s7, v30
	v_mul_lo_u32 v64, v21, s10
	v_mad_u32_u24 v21, v29, s21, v240
	v_add_lshl_u32 v65, v21, v25, 1
	v_add_lshl_u32 v67, v21, v28, 1
	v_mad_u32_u24 v21, v29, s21, v241
	v_add_lshl_u32 v70, v21, v25, 1
	v_add_lshl_u32 v71, v21, v28, 1
	v_mad_u32_u24 v21, v29, s21, v242
	s_or_b32 s6, s6, 16
	v_add_lshl_u32 v72, v21, v25, 1
	v_add_lshl_u32 v73, v21, v28, 1
	v_or_b32_e32 v21, s6, v24
	v_mul_lo_u32 v21, v21, s21
	v_ashrrev_i32_e32 v51, 10, v20
	v_bfe_u32 v33, v20, 3, 7
	v_add_lshl_u32 v74, v21, v25, 1
	v_add_lshl_u32 v75, v21, v28, 1
	v_add_u32_e32 v21, s6, v30
	v_mul_u32_u24_e32 v22, 0x48, v29
	v_mul_lo_u32 v76, v21, s10
	v_lshl_or_b32 v21, v51, 7, v33
	v_and_b32_e32 v32, 56, v46
	v_add_lshl_u32 v62, v22, v25, 1
	v_add_lshl_u32 v63, v22, v28, 1
	v_mul_lo_u32 v21, v21, s21
	v_lshlrev_b32_e32 v22, 7, v33
	v_mov_b32_e32 v23, v69
	v_lshl_add_u32 v43, v24, 1, s92
	v_add_lshl_u32 v77, v21, v32, 1
	v_lshl_add_u64 v[22:23], s[0:1], 0, v[22:23]
	v_lshlrev_b32_e32 v24, 1, v32
	v_mov_b32_e32 v25, v69
	v_add_u32_e32 v21, 0x200, v20
	v_lshl_add_u64 v[28:29], v[22:23], 0, v[24:25]
	v_ashrrev_i32_e32 v52, 10, v21
	v_bfe_u32 v22, v21, 3, 7
	v_cmp_gt_u32_e64 s[8:9], s90, v21
	v_lshl_or_b32 v21, v52, 7, v22
	v_mul_lo_u32 v21, v21, s21
	v_add_lshl_u32 v78, v21, v32, 1
	v_add_u32_e32 v21, 0x400, v20
	v_ashrrev_i32_e32 v53, 10, v21
	v_mul_lo_u32 v36, v47, s10
	s_movk_i32 s2, 0x100
	v_lshlrev_b32_e32 v22, 7, v22
	v_mov_b32_e32 v23, v69
	s_movk_i32 s10, 0xfbff
	v_lshl_or_b32 v21, v53, 7, v33
	v_cmp_gt_i32_e64 s[2:3], s2, v20
	v_cmp_gt_u32_e64 s[6:7], s90, v20
	v_lshl_add_u64 v[22:23], s[0:1], 0, v[22:23]
	v_cmp_lt_u32_e64 s[10:11], s10, v20
	v_mul_lo_u32 v21, v21, s21
	v_add_u32_e32 v20, 0x600, v20
	v_lshl_add_u64 v[30:31], v[22:23], 0, v[24:25]
	v_add_lshl_u32 v22, v21, v32, 1
	v_ashrrev_i32_e32 v54, 10, v20
	v_bfe_u32 v21, v20, 3, 7
	v_cmp_gt_u32_e64 s[12:13], s90, v20
	v_lshl_or_b32 v20, v54, 7, v21
	v_mul_lo_u32 v20, v20, s21
	v_add_lshl_u32 v23, v20, v32, 1
	v_lshlrev_b32_e32 v20, 7, v21
	v_mov_b32_e32 v21, v69
	v_lshl_add_u64 v[20:21], s[0:1], 0, v[20:21]
	s_lshl_b32 s0, s25, 6
	s_mul_i32 s15, s20, 0x480
	v_lshl_add_u64 v[32:33], v[20:21], 0, v[24:25]
	s_add_i32 s40, s0, 0x1300
	s_lshl_b32 s0, s25, 12
	v_add_u32_e32 v20, 0, v41
	v_lshl_add_u64 v[34:35], s[16:17], 0, v[68:69]
	s_mul_i32 s21, s30, 0x108
	s_lshl_b32 s38, s25, 1
	s_sub_i32 s39, 0, s25
	s_add_i32 s41, s0, 0x40000
	v_add_u32_e32 v55, v37, v36
	v_add_u32_e32 v56, v38, v39
	v_add_u32_e32 v57, 0, v40
	v_add_u32_e32 v58, 0x1b000, v20
	v_add_u32_e32 v59, s15, v42
	v_lshlrev_b32_e32 v68, 1, v19
	s_lshl_b32 s24, s14, 1
	v_lshlrev_b32_e32 v36, 1, v18
	v_add_u32_e32 v60, 0, v44
	v_add_u32_e32 v61, 0, v45
	v_add_u32_e32 v62, 0, v62
	v_add_u32_e32 v63, 0, v63
	v_add_u32_e32 v64, v43, v64
	v_add_u32_e32 v65, 0, v65
	v_add_u32_e32 v67, 0, v67
	v_add_u32_e32 v70, 0, v70
	v_add_u32_e32 v71, 0, v71
	v_add_u32_e32 v72, 0, v72
	v_add_u32_e32 v73, 0, v73
	v_add_u32_e32 v74, 0, v74
	v_add_u32_e32 v75, 0, v75
	v_add_u32_e32 v76, v43, v76
	v_add_u32_e32 v77, s92, v77
	v_add_u32_e32 v78, s92, v78
	v_add_u32_e32 v79, s92, v22
	v_add_u32_e32 v80, s92, v23
	v_mov_b32_e32 v194, 0x23f70
	v_mov_b32_e32 v196, 0x23f78
	ds_read_b64 v[194:195], v194
	ds_read_b64 v[196:197], v196
	s_waitcnt lgkmcnt(0)
	v_readfirstlane_b32 vcc_lo, v194
	v_readfirstlane_b32 vcc_hi, v195
	v_readfirstlane_b32 s0, v196
	v_readfirstlane_b32 s1, v197
	s_nop 3
	v_writelane_b32 v246, vcc_lo, 51
	v_writelane_b32 v246, vcc_hi, 52
	v_writelane_b32 v246, s0, 53
	v_writelane_b32 v246, s1, 54
	v_and_b32_e32 v194, 63, v0
	v_lshrrev_b32_e32 v195, 6, v0
	v_lshrrev_b32_e32 v188, 3, v194
	v_lshlrev_b32_e32 v188, 14, v188
	v_lshl_add_u32 v188, v195, 7, v188
	v_and_b32_e32 v189, 7, v194
	v_lshl_add_u32 v188, v189, 4, v188
	v_lshrrev_b32_e32 v192, 2, v195
	v_lshlrev_b32_e32 v192, 18, v192
	v_and_b32_e32 v190, 3, v195
	v_lshl_add_u32 v192, v190, 12, v192
	v_lshl_add_u32 v192, v189, 9, v192
	v_lshrrev_b32_e32 v190, 3, v194
	v_lshl_add_u32 v192, v190, 4, v192
	v_add_u32_e32 v189, 0x1000, v188
	v_add_u32_e32 v190, 0x2000, v188
	v_add_u32_e32 v191, 0x3000, v188
	s_add_i32 vcc_lo, s95, 0x700
	v_writelane_b32 v246, vcc_lo, 48
	s_mov_b32 vcc_lo, 8
	v_writelane_b32 v246, vcc_lo, 50
	s_mov_b32 vcc_lo, 0
	v_writelane_b32 v246, vcc_lo, 49
	s_branch .LBB0_499

.LBB0_498:
	s_waitcnt lgkmcnt(0)
	s_barrier
	ds_read_b128 v[18:21], v60 offset:54272
	ds_read_b128 v[22:25], v61 offset:54272
	ds_read_b128 v[38:41], v62 offset:17408
	ds_read_b128 v[42:45], v63 offset:17408
	s_mul_i32 s0, s45, 0x84
	s_waitcnt lgkmcnt(1)
	v_mfma_f32_16x16x32_bf16 v[38:41], v[18:21], v[38:41], 0
	s_lshl_b32 s1, s30, 1
	s_lshl_b32 s25, s45, 3
	s_or_b32 s1, s25, s1
	s_waitcnt lgkmcnt(0)
	v_mfma_f32_16x16x32_bf16 v[38:41], v[22:25], v[42:45], v[38:41]
	s_cmp_gt_i32 s44, 3
	s_cselect_b32 s25, 0x87, 3
	s_add_i32 s25, s25, s0
	s_addk_i32 s38, 0x80
	s_addk_i32 s40, 0x1000
	s_nop 2
	v_cvt_pk_bf16_f32 v37, v38, s0
	ds_write_b16 v64, v37
	v_cvt_pk_bf16_f32 v37, v39, s0
	ds_write_b16 v64, v37 offset:144
	v_cvt_pk_bf16_f32 v37, v40, s0
	ds_write_b16 v64, v37 offset:288
	v_cvt_pk_bf16_f32 v37, v41, s0
	ds_write_b16 v64, v37 offset:432
	ds_read_b128 v[38:41], v65 offset:17408
	ds_read_b128 v[42:45], v67 offset:17408
	s_waitcnt lgkmcnt(1)
	v_mfma_f32_16x16x32_bf16 v[38:41], v[18:21], v[38:41], 0
	s_add_i32 s41, s41, 0x40000
	s_and_b64 vcc, exec, s[14:15]
	s_waitcnt lgkmcnt(0)
	v_mfma_f32_16x16x32_bf16 v[38:41], v[22:25], v[42:45], v[38:41]
	s_nop 7
	v_cvt_pk_bf16_f32 v37, v38, s0
	ds_write_b16 v64, v37 offset:32
	v_cvt_pk_bf16_f32 v37, v39, s0
	ds_write_b16 v64, v37 offset:176
	v_cvt_pk_bf16_f32 v37, v40, s0
	ds_write_b16 v64, v37 offset:320
	v_cvt_pk_bf16_f32 v37, v41, s0
	ds_write_b16 v64, v37 offset:464
	ds_read_b128 v[38:41], v70 offset:17408
	ds_read_b128 v[42:45], v71 offset:17408
	s_waitcnt lgkmcnt(1)
	v_mfma_f32_16x16x32_bf16 v[38:41], v[18:21], v[38:41], 0
	s_waitcnt lgkmcnt(0)
	v_mfma_f32_16x16x32_bf16 v[38:41], v[22:25], v[42:45], v[38:41]
	s_nop 7
	v_cvt_pk_bf16_f32 v37, v38, s0
	ds_write_b16 v64, v37 offset:64
	v_cvt_pk_bf16_f32 v37, v39, s0
	ds_write_b16 v64, v37 offset:208
	v_cvt_pk_bf16_f32 v37, v40, s0
	ds_write_b16 v64, v37 offset:352
	v_cvt_pk_bf16_f32 v37, v41, s0
	ds_write_b16 v64, v37 offset:496
	ds_read_b128 v[38:41], v72 offset:17408
	ds_read_b128 v[42:45], v73 offset:17408
	s_waitcnt lgkmcnt(1)
	v_mfma_f32_16x16x32_bf16 v[18:21], v[18:21], v[38:41], 0
	s_waitcnt lgkmcnt(0)
	v_mfma_f32_16x16x32_bf16 v[18:21], v[22:25], v[42:45], v[18:21]
	s_nop 7
	v_cvt_pk_bf16_f32 v18, v18, s0
	ds_write_b16 v64, v18 offset:96
	v_cvt_pk_bf16_f32 v18, v19, s0
	ds_write_b16 v64, v18 offset:240
	v_cvt_pk_bf16_f32 v18, v20, s0
	ds_write_b16 v64, v18 offset:384
	v_cvt_pk_bf16_f32 v18, v21, s0
	ds_write_b16 v64, v18 offset:528
	ds_read_b128 v[18:21], v74 offset:54272
	ds_read_b128 v[22:25], v75 offset:54272
	ds_read_b128 v[38:41], v62 offset:17408
	ds_read_b128 v[42:45], v63 offset:17408
	s_waitcnt lgkmcnt(1)
	v_mfma_f32_16x16x32_bf16 v[38:41], v[18:21], v[38:41], 0
	s_waitcnt lgkmcnt(0)
	v_mfma_f32_16x16x32_bf16 v[38:41], v[22:25], v[42:45], v[38:41]
	s_nop 7
	v_cvt_pk_bf16_f32 v37, v38, s0
	ds_write_b16 v76, v37
	v_cvt_pk_bf16_f32 v37, v39, s0
	ds_write_b16 v76, v37 offset:144
	v_cvt_pk_bf16_f32 v37, v40, s0
	ds_write_b16 v76, v37 offset:288
	v_cvt_pk_bf16_f32 v37, v41, s0
	ds_write_b16 v76, v37 offset:432
	ds_read_b128 v[38:41], v65 offset:17408
	ds_read_b128 v[42:45], v67 offset:17408
	s_waitcnt lgkmcnt(1)
	v_mfma_f32_16x16x32_bf16 v[38:41], v[18:21], v[38:41], 0
	s_waitcnt lgkmcnt(0)
	v_mfma_f32_16x16x32_bf16 v[38:41], v[22:25], v[42:45], v[38:41]
	s_nop 7
	v_cvt_pk_bf16_f32 v37, v38, s0
	ds_write_b16 v76, v37 offset:32
	v_cvt_pk_bf16_f32 v37, v39, s0
	ds_write_b16 v76, v37 offset:176
	v_cvt_pk_bf16_f32 v37, v40, s0
	ds_write_b16 v76, v37 offset:320
	v_cvt_pk_bf16_f32 v37, v41, s0
	ds_write_b16 v76, v37 offset:464
	ds_read_b128 v[38:41], v70 offset:17408
	ds_read_b128 v[42:45], v71 offset:17408
	s_waitcnt lgkmcnt(1)
	v_mfma_f32_16x16x32_bf16 v[38:41], v[18:21], v[38:41], 0
	s_waitcnt lgkmcnt(0)
	v_mfma_f32_16x16x32_bf16 v[38:41], v[22:25], v[42:45], v[38:41]
	s_nop 7
	v_cvt_pk_bf16_f32 v37, v38, s0
	ds_write_b16 v76, v37 offset:64
	v_cvt_pk_bf16_f32 v37, v39, s0
	ds_write_b16 v76, v37 offset:208
	v_cvt_pk_bf16_f32 v37, v40, s0
	ds_write_b16 v76, v37 offset:352
	v_cvt_pk_bf16_f32 v37, v41, s0
	ds_write_b16 v76, v37 offset:496
	ds_read_b128 v[38:41], v72 offset:17408
	ds_read_b128 v[42:45], v73 offset:17408
	s_waitcnt lgkmcnt(1)
	v_mfma_f32_16x16x32_bf16 v[18:21], v[18:21], v[38:41], 0
	s_waitcnt lgkmcnt(0)
	v_mfma_f32_16x16x32_bf16 v[18:21], v[22:25], v[42:45], v[18:21]
	v_mov_b32_e32 v25, s44
	s_nop 6
	v_cvt_pk_bf16_f32 v18, v18, s0
	ds_write_b16 v76, v18 offset:96
	v_cvt_pk_bf16_f32 v18, v19, s0
	ds_write_b16 v76, v18 offset:240
	v_cvt_pk_bf16_f32 v18, v20, s0
	ds_write_b16 v76, v18 offset:384
	v_cvt_pk_bf16_f32 v18, v21, s0
	s_add_i32 s0, s39, s25
	v_mov_b32_e32 v24, s0
	ds_write_b16 v76, v18 offset:528
	v_cndmask_b32_e64 v18, v24, v25, s[6:7]
	s_waitcnt lgkmcnt(0)
	s_barrier
	v_add_u32_e32 v20, s1, v51
	v_ashrrev_i32_e32 v19, 31, v18
	s_movk_i32 s0, 0x84
	v_mad_i64_i32 v[22:23], s[26:27], v20, s0, v[18:19]
	ds_read_b128 v[18:21], v77
	v_lshlrev_b64 v[22:23], 14, v[22:23]
	v_lshl_add_u64 v[22:23], v[28:29], 0, v[22:23]
	s_sub_i32 s39, s39, 64
	s_mov_b32 s25, s48
	s_waitcnt lgkmcnt(0)
	global_store_dwordx4 v[22:23], v[18:21], off
	s_nop 1
	v_cndmask_b32_e64 v18, v24, v25, s[8:9]
	v_add_u32_e32 v20, s1, v52
	v_ashrrev_i32_e32 v19, 31, v18
	v_mad_i64_i32 v[22:23], s[26:27], v20, s0, v[18:19]
	ds_read_b128 v[18:21], v78
	v_lshlrev_b64 v[22:23], 14, v[22:23]
	v_lshl_add_u64 v[22:23], v[30:31], 0, v[22:23]
	s_waitcnt lgkmcnt(0)
	global_store_dwordx4 v[22:23], v[18:21], off
	s_nop 1
	v_cndmask_b32_e64 v18, v24, v25, s[10:11]
	v_add_u32_e32 v20, s1, v53
	v_ashrrev_i32_e32 v19, 31, v18
	v_mad_i64_i32 v[22:23], s[26:27], v20, s0, v[18:19]
	ds_read_b128 v[18:21], v79
	v_lshlrev_b64 v[22:23], 14, v[22:23]
	v_lshl_add_u64 v[22:23], v[28:29], 0, v[22:23]
	s_waitcnt lgkmcnt(0)
	global_store_dwordx4 v[22:23], v[18:21], off
	s_nop 1
	v_cndmask_b32_e64 v18, v24, v25, s[12:13]
	v_add_u32_e32 v20, s1, v54
	v_ashrrev_i32_e32 v19, 31, v18
	v_mad_i64_i32 v[22:23], s[0:1], v20, s0, v[18:19]
	ds_read_b128 v[18:21], v80
	v_lshlrev_b64 v[22:23], 14, v[22:23]
	v_lshl_add_u64 v[22:23], v[32:33], 0, v[22:23]
	s_waitcnt lgkmcnt(0)
	global_store_dwordx4 v[22:23], v[18:21], off
	v_readlane_b32 s26, v246, 49
	s_nop 1
	s_cmp_eq_u32 s26, 0
	s_cbranch_scc1 .Lc1_cskip
	v_readlane_b32 s0, v246, 40
	v_readlane_b32 s1, v246, 41
	s_mov_b32 s26, 0
	v_writelane_b32 v246, s26, 49
	s_mov_b32 s26, 0x42000000
	s_mov_b32 s27, 0x42000000
	s_waitcnt vmcnt(0)
	v_pk_mul_f32 v[108:109], v[108:109], s[26:27] op_sel_hi:[1,0]
	v_pk_mul_f32 v[110:111], v[110:111], s[26:27] op_sel_hi:[1,0]
	v_pk_mul_f32 v[112:113], v[112:113], s[26:27] op_sel_hi:[1,0]
	v_pk_mul_f32 v[114:115], v[114:115], s[26:27] op_sel_hi:[1,0]
	v_pk_mul_f32 v[116:117], v[116:117], s[26:27] op_sel_hi:[1,0]
	v_pk_mul_f32 v[118:119], v[118:119], s[26:27] op_sel_hi:[1,0]
	v_pk_mul_f32 v[120:121], v[120:121], s[26:27] op_sel_hi:[1,0]
	v_pk_mul_f32 v[122:123], v[122:123], s[26:27] op_sel_hi:[1,0]
	v_pk_mul_f32 v[124:125], v[124:125], s[26:27] op_sel_hi:[1,0]
	v_pk_mul_f32 v[126:127], v[126:127], s[26:27] op_sel_hi:[1,0]
	v_pk_mul_f32 v[128:129], v[128:129], s[26:27] op_sel_hi:[1,0]
	v_pk_mul_f32 v[130:131], v[130:131], s[26:27] op_sel_hi:[1,0]
	v_pk_mul_f32 v[132:133], v[132:133], s[26:27] op_sel_hi:[1,0]
	v_pk_mul_f32 v[134:135], v[134:135], s[26:27] op_sel_hi:[1,0]
	v_pk_mul_f32 v[136:137], v[136:137], s[26:27] op_sel_hi:[1,0]
	v_pk_mul_f32 v[138:139], v[138:139], s[26:27] op_sel_hi:[1,0]
	v_pk_mul_f32 v[140:141], v[140:141], s[26:27] op_sel_hi:[1,0]
	v_pk_mul_f32 v[142:143], v[142:143], s[26:27] op_sel_hi:[1,0]
	v_pk_mul_f32 v[144:145], v[144:145], s[26:27] op_sel_hi:[1,0]
	v_pk_mul_f32 v[146:147], v[146:147], s[26:27] op_sel_hi:[1,0]
	v_pk_mul_f32 v[148:149], v[148:149], s[26:27] op_sel_hi:[1,0]
	v_pk_mul_f32 v[150:151], v[150:151], s[26:27] op_sel_hi:[1,0]
	v_pk_mul_f32 v[152:153], v[152:153], s[26:27] op_sel_hi:[1,0]
	v_pk_mul_f32 v[154:155], v[154:155], s[26:27] op_sel_hi:[1,0]
	v_pk_mul_f32 v[156:157], v[156:157], s[26:27] op_sel_hi:[1,0]
	v_pk_mul_f32 v[158:159], v[158:159], s[26:27] op_sel_hi:[1,0]
	v_pk_mul_f32 v[160:161], v[160:161], s[26:27] op_sel_hi:[1,0]
	v_pk_mul_f32 v[162:163], v[162:163], s[26:27] op_sel_hi:[1,0]
	v_pk_mul_f32 v[164:165], v[164:165], s[26:27] op_sel_hi:[1,0]
	v_pk_mul_f32 v[166:167], v[166:167], s[26:27] op_sel_hi:[1,0]
	v_pk_mul_f32 v[168:169], v[168:169], s[26:27] op_sel_hi:[1,0]
	v_pk_mul_f32 v[170:171], v[170:171], s[26:27] op_sel_hi:[1,0]
	v_cvt_pk_fp8_f32 v172, v108, v112
	v_cvt_pk_fp8_f32 v173, v124, v128
	v_cvt_pk_fp8_f32 v174, v140, v144
	v_cvt_pk_fp8_f32 v175, v156, v160
	v_cvt_pk_fp8_f32 v176, v109, v113
	v_cvt_pk_fp8_f32 v177, v125, v129
	v_cvt_pk_fp8_f32 v178, v141, v145
	v_cvt_pk_fp8_f32 v179, v157, v161
	v_cvt_pk_fp8_f32 v180, v110, v114
	v_cvt_pk_fp8_f32 v181, v126, v130
	v_cvt_pk_fp8_f32 v182, v142, v146
	v_cvt_pk_fp8_f32 v183, v158, v162
	v_cvt_pk_fp8_f32 v184, v111, v115
	v_cvt_pk_fp8_f32 v185, v127, v131
	v_cvt_pk_fp8_f32 v186, v143, v147
	v_cvt_pk_fp8_f32 v187, v159, v163
	v_cvt_pk_fp8_f32 v172, v116, v120 op_sel:[0,0,1]
	v_cvt_pk_fp8_f32 v173, v132, v136 op_sel:[0,0,1]
	v_cvt_pk_fp8_f32 v174, v148, v152 op_sel:[0,0,1]
	v_cvt_pk_fp8_f32 v175, v164, v168 op_sel:[0,0,1]
	v_cvt_pk_fp8_f32 v176, v117, v121 op_sel:[0,0,1]
	v_cvt_pk_fp8_f32 v177, v133, v137 op_sel:[0,0,1]
	v_cvt_pk_fp8_f32 v178, v149, v153 op_sel:[0,0,1]
	v_cvt_pk_fp8_f32 v179, v165, v169 op_sel:[0,0,1]
	v_cvt_pk_fp8_f32 v180, v118, v122 op_sel:[0,0,1]
	v_cvt_pk_fp8_f32 v181, v134, v138 op_sel:[0,0,1]
	v_cvt_pk_fp8_f32 v182, v150, v154 op_sel:[0,0,1]
	v_cvt_pk_fp8_f32 v183, v166, v170 op_sel:[0,0,1]
	v_cvt_pk_fp8_f32 v184, v119, v123 op_sel:[0,0,1]
	v_cvt_pk_fp8_f32 v185, v135, v139 op_sel:[0,0,1]
	v_cvt_pk_fp8_f32 v186, v151, v155 op_sel:[0,0,1]
	v_cvt_pk_fp8_f32 v187, v167, v171 op_sel:[0,0,1]
	global_store_dwordx4 v192, v[172:175], s[0:1]
	global_store_dwordx4 v192, v[176:179], s[0:1] offset:128
	global_store_dwordx4 v192, v[180:183], s[0:1] offset:256
	global_store_dwordx4 v192, v[184:187], s[0:1] offset:384
.Lc1_cskip:
	s_cbranch_vccnz .LBB0_512

.LBB0_501:
	s_or_b64 exec, exec, s[0:1]
	s_waitcnt lgkmcnt(0)
	s_barrier
	v_writelane_b32 v246, s24, 0
	v_writelane_b32 v246, s25, 1
	v_writelane_b32 v246, s28, 2
	v_writelane_b32 v246, s29, 3
	v_writelane_b32 v246, s30, 4
	v_writelane_b32 v246, s31, 5
	s_nop 1
	v_readlane_b32 s26, v246, 48
	v_readlane_b32 s27, v246, 50
	s_nop 1
	s_cmp_eq_u32 s27, 0
	s_cbranch_scc1 .Lc1_iskip
	s_add_i32 s27, s27, -1
	v_writelane_b32 v246, s27, 50
	s_add_i32 s27, s26, 0x100
	v_writelane_b32 v246, s27, 48
	v_readlane_b32 s28, v246, 51
	v_readlane_b32 s29, v246, 52
	v_readlane_b32 s30, v246, 53
	v_readlane_b32 s31, v246, 54
	v_readlane_b32 vcc_lo, v247, 34
	s_nop 1
	s_and_b32 vcc_lo, vcc_lo, 0x10000000
	s_and_b32 s14, s26, 0x7ff
	s_lshr_b32 s15, s14, 3
	s_and_b32 s14, s14, 7
	s_lshr_b32 s27, s26, 11
	s_lshl_b32 s24, s15, 19
	s_lshl_b32 s25, s14, 15
	s_add_i32 s24, s24, s25
	s_lshl_b32 s25, s27, 14
	s_add_i32 s24, s24, s25
	s_add_u32 s24, s24, 0x94c000
	s_add_u32 s24, s24, s42
	s_addc_u32 s25, s43, 0
	s_cmp_eq_u32 s27, 0
	s_cselect_b32 s0, s28, s30
	s_cselect_b32 s1, s29, s31
	s_lshl_b32 s15, s15, 20
	s_lshl_b32 s14, s14, 17
	s_add_i32 s15, s15, s14
	s_add_i32 s15, s15, vcc_lo
	s_add_u32 s0, s0, s15
	s_addc_u32 s1, s1, 0
	global_load_dwordx4 v[108:111], v188, s[0:1] nt
	global_load_dwordx4 v[112:115], v188, s[0:1] offset:1024 nt
	global_load_dwordx4 v[116:119], v188, s[0:1] offset:2048 nt
	global_load_dwordx4 v[120:123], v188, s[0:1] offset:3072 nt
	global_load_dwordx4 v[124:127], v189, s[0:1] nt
	global_load_dwordx4 v[128:131], v189, s[0:1] offset:1024 nt
	global_load_dwordx4 v[132:135], v189, s[0:1] offset:2048 nt
	global_load_dwordx4 v[136:139], v189, s[0:1] offset:3072 nt
	global_load_dwordx4 v[140:143], v190, s[0:1] nt
	global_load_dwordx4 v[144:147], v190, s[0:1] offset:1024 nt
	global_load_dwordx4 v[148:151], v190, s[0:1] offset:2048 nt
	global_load_dwordx4 v[152:155], v190, s[0:1] offset:3072 nt
	global_load_dwordx4 v[156:159], v191, s[0:1] nt
	global_load_dwordx4 v[160:163], v191, s[0:1] offset:1024 nt
	global_load_dwordx4 v[164:167], v191, s[0:1] offset:2048 nt
	global_load_dwordx4 v[168:171], v191, s[0:1] offset:3072 nt
	v_writelane_b32 v246, s24, 40
	v_writelane_b32 v246, s25, 41
	s_mov_b32 s27, 1
	v_writelane_b32 v246, s27, 49
.Lc1_iskip:
	v_readlane_b32 s24, v246, 0
	v_readlane_b32 s25, v246, 1
	v_readlane_b32 s28, v246, 2
	v_readlane_b32 s29, v246, 3
	v_readlane_b32 s30, v246, 4
	v_readlane_b32 s31, v246, 5
	s_nop 4
	v_mov_b32_e32 v37, s31
	ds_read2_b32 v[40:41], v57 offset1:1
	ds_read2_b32 v[44:45], v57 offset0:2 offset1:3
	ds_read2_b32 v[42:43], v57 offset0:4 offset1:5
	ds_read2_b32 v[38:39], v57 offset0:6 offset1:7
	ds_read_b128 v[18:21], v37 offset:16896
	ds_read_b128 v[22:25], v37 offset:16912
	ds_read_b128 v[82:85], v37 offset:8704
	ds_read_b128 v[86:89], v37 offset:8720
	s_mul_hi_i32 s0, s25, 0x3e0f83e1
	s_lshr_b32 s1, s0, 31
	s_ashr_i32 s45, s0, 5
	s_waitcnt lgkmcnt(1)
	v_fma_f32 v81, v40, v82, v18
	s_waitcnt lgkmcnt(0)
	v_fma_f32 v98, v40, v86, v22
	v_fma_f32 v99, v40, v83, v19
	v_fma_f32 v100, v40, v87, v23
	v_fma_f32 v20, v40, v84, v20
	v_fma_f32 v101, v40, v88, v24
	v_fmac_f32_e32 v21, v40, v85
	v_fmac_f32_e32 v25, v40, v89
	ds_read_b128 v[82:85], v37 offset:8976
	ds_read_b128 v[86:89], v37 offset:8960
	s_add_i32 s45, s45, s1
	s_mul_i32 s0, s45, 0xffffff7c
	s_add_i32 s44, s25, s0
	s_waitcnt lgkmcnt(1)
	v_fmac_f32_e32 v98, v41, v82
	s_waitcnt lgkmcnt(0)
	v_fmac_f32_e32 v81, v41, v86
	v_fmac_f32_e32 v99, v41, v87
	v_fmac_f32_e32 v100, v41, v83
	v_fmac_f32_e32 v20, v41, v88
	v_fmac_f32_e32 v101, v41, v84
	v_fmac_f32_e32 v21, v41, v89
	v_fmac_f32_e32 v25, v41, v85
	ds_read_b128 v[82:85], v37 offset:9232
	ds_read_b128 v[86:89], v37 offset:9216
	s_mul_i32 s0, s45, 0x318
	s_add_i32 s1, s21, s38
	s_add_i32 s26, s1, s0
	s_waitcnt lgkmcnt(1)
	v_fmac_f32_e32 v98, v44, v82
	s_waitcnt lgkmcnt(0)
	v_fmac_f32_e32 v81, v44, v86
	v_fmac_f32_e32 v99, v44, v87
	v_fmac_f32_e32 v100, v44, v83
	v_fmac_f32_e32 v20, v44, v88
	v_fmac_f32_e32 v101, v44, v84
	v_fmac_f32_e32 v21, v44, v89
	v_fmac_f32_e32 v25, v44, v85
	ds_read_b128 v[82:85], v37 offset:9488
	ds_read_b128 v[86:89], v37 offset:9472
	s_ashr_i32 s27, s26, 31
	s_lshl_b64 s[0:1], s[26:27], 13
	s_waitcnt lgkmcnt(1)
	v_fmac_f32_e32 v98, v45, v82
	s_waitcnt lgkmcnt(0)
	v_fmac_f32_e32 v81, v45, v86
	v_fmac_f32_e32 v99, v45, v87
	v_fmac_f32_e32 v100, v45, v83
	v_fmac_f32_e32 v20, v45, v88
	v_fmac_f32_e32 v101, v45, v84
	v_fmac_f32_e32 v21, v45, v89
	v_fmac_f32_e32 v25, v45, v85
	ds_read2_b32 v[18:19], v57 offset0:14 offset1:15
	ds_read2_b32 v[22:23], v57 offset0:12 offset1:13
	ds_read2_b32 v[40:41], v57 offset0:10 offset1:11
	ds_read2_b32 v[44:45], v57 offset0:8 offset1:9
	ds_read_b128 v[82:85], v37 offset:9728
	ds_read_b128 v[86:89], v37 offset:9744
	s_waitcnt lgkmcnt(1)
	v_fmac_f32_e32 v81, v42, v82
	s_waitcnt lgkmcnt(0)
	v_fmac_f32_e32 v98, v42, v86
	v_fmac_f32_e32 v99, v42, v83
	v_fmac_f32_e32 v100, v42, v87
	v_fmac_f32_e32 v20, v42, v84
	v_fmac_f32_e32 v101, v42, v88
	v_fmac_f32_e32 v21, v42, v85
	v_fmac_f32_e32 v25, v42, v89
	ds_read_b128 v[82:85], v37 offset:10000
	ds_read_b128 v[86:89], v37 offset:9984
	s_waitcnt lgkmcnt(1)
	v_fmac_f32_e32 v98, v43, v82
	s_waitcnt lgkmcnt(0)
	v_fmac_f32_e32 v81, v43, v86
	v_fmac_f32_e32 v99, v43, v87
	v_fmac_f32_e32 v100, v43, v83
	v_fmac_f32_e32 v20, v43, v88
	v_fmac_f32_e32 v101, v43, v84
	v_fmac_f32_e32 v21, v43, v89
	v_fmac_f32_e32 v25, v43, v85
	ds_read_b128 v[82:85], v37 offset:10256
	ds_read_b128 v[86:89], v37 offset:10240
	s_waitcnt lgkmcnt(1)
	v_fmac_f32_e32 v98, v38, v82
	s_waitcnt lgkmcnt(0)
	v_fmac_f32_e32 v81, v38, v86
	v_fmac_f32_e32 v99, v38, v87
	v_fmac_f32_e32 v100, v38, v83
	v_fmac_f32_e32 v20, v38, v88
	v_fmac_f32_e32 v101, v38, v84
	v_fmac_f32_e32 v21, v38, v89
	v_fmac_f32_e32 v25, v38, v85
	ds_read_b128 v[82:85], v37 offset:10512
	ds_read_b128 v[86:89], v37 offset:10496
	s_waitcnt lgkmcnt(1)
	v_fmac_f32_e32 v98, v39, v82
	s_waitcnt lgkmcnt(0)
	v_fmac_f32_e32 v81, v39, v86
	v_fmac_f32_e32 v99, v39, v87
	v_fmac_f32_e32 v100, v39, v83
	v_fmac_f32_e32 v20, v39, v88
	v_fmac_f32_e32 v101, v39, v84
	v_fmac_f32_e32 v21, v39, v89
	v_fmac_f32_e32 v25, v39, v85
	ds_read_b128 v[82:85], v37 offset:10752
	ds_read_b128 v[86:89], v37 offset:10768
	ds_read_b128 v[90:93], v37 offset:11024
	ds_read_b128 v[94:97], v37 offset:11008
	s_waitcnt lgkmcnt(3)
	v_mov_b32_e32 v24, v82
	s_waitcnt lgkmcnt(2)
	v_mov_b32_e32 v38, v89
	s_waitcnt lgkmcnt(1)
	v_mov_b32_e32 v39, v93
	v_pk_mul_f32 v[38:39], v[44:45], v[38:39]
	v_mov_b32_e32 v89, v92
	v_add_f32_e32 v38, v25, v38
	s_waitcnt lgkmcnt(0)
	v_mov_b32_e32 v25, v94
	v_pk_mul_f32 v[24:25], v[44:45], v[24:25]
	v_mov_b32_e32 v94, v83
	v_add_f32_e32 v24, v81, v24
	v_add_f32_e32 v81, v24, v25
	v_mov_b32_e32 v24, v86
	v_mov_b32_e32 v25, v90
	v_pk_mul_f32 v[24:25], v[44:45], v[24:25]
	v_mov_b32_e32 v90, v87
	v_add_f32_e32 v24, v98, v24
	v_add_f32_e32 v98, v25, v24
	v_pk_mul_f32 v[24:25], v[44:45], v[94:95]
	s_nop 0
	v_add_f32_e32 v24, v99, v24
	v_add_f32_e32 v94, v24, v25
	v_pk_mul_f32 v[24:25], v[44:45], v[90:91]
	s_nop 0
	v_add_f32_e32 v24, v100, v24
	v_add_f32_e32 v95, v25, v24
	v_mov_b32_e32 v24, v84
	v_mov_b32_e32 v25, v96
	v_pk_mul_f32 v[24:25], v[44:45], v[24:25]
	v_mov_b32_e32 v96, v85
	v_add_f32_e32 v20, v20, v24
	v_add_f32_e32 v99, v20, v25
	v_pk_mul_f32 v[24:25], v[44:45], v[88:89]
	s_nop 0
	v_add_f32_e32 v20, v101, v24
	v_add_f32_e32 v100, v25, v20
	v_pk_mul_f32 v[24:25], v[44:45], v[96:97]
	ds_read_b128 v[42:45], v37 offset:11280
	ds_read_b128 v[82:85], v37 offset:11264
	ds_read_b128 v[86:89], v37 offset:11536
	ds_read_b128 v[90:93], v37 offset:11520
	v_add_f32_e32 v20, v21, v24
	v_add_f32_e32 v96, v20, v25
	s_waitcnt lgkmcnt(3)
	v_mov_b32_e32 v20, v45
	s_waitcnt lgkmcnt(1)
	v_mov_b32_e32 v21, v89
	v_add_f32_e32 v24, v39, v38
	v_pk_mul_f32 v[20:21], v[40:41], v[20:21]
	s_waitcnt lgkmcnt(0)
	v_mov_b32_e32 v25, v90
	v_add_f32_e32 v20, v24, v20
	v_mov_b32_e32 v24, v82
	v_pk_mul_f32 v[24:25], v[40:41], v[24:25]
	v_mov_b32_e32 v90, v83
	v_add_f32_e32 v24, v81, v24
	v_add_f32_e32 v81, v24, v25
	v_mov_b32_e32 v24, v42
	v_mov_b32_e32 v25, v86
	v_pk_mul_f32 v[24:25], v[40:41], v[24:25]
	v_mov_b32_e32 v86, v43
	v_add_f32_e32 v24, v98, v24
	v_add_f32_e32 v97, v24, v25
	v_pk_mul_f32 v[24:25], v[40:41], v[90:91]
	v_mov_b32_e32 v45, v88
	v_add_f32_e32 v24, v94, v24
	v_add_f32_e32 v90, v24, v25
	v_pk_mul_f32 v[24:25], v[40:41], v[86:87]
	s_nop 0
	v_add_f32_e32 v24, v95, v24
	v_add_f32_e32 v91, v24, v25
	v_mov_b32_e32 v24, v84
	v_mov_b32_e32 v25, v92
	v_pk_mul_f32 v[24:25], v[40:41], v[24:25]
	v_mov_b32_e32 v92, v85
	v_add_f32_e32 v24, v99, v24
	v_add_f32_e32 v94, v24, v25
	v_pk_mul_f32 v[24:25], v[40:41], v[44:45]
	s_nop 0
	v_add_f32_e32 v24, v100, v24
	v_add_f32_e32 v95, v24, v25
	v_pk_mul_f32 v[24:25], v[40:41], v[92:93]
	ds_read_b128 v[38:41], v37 offset:11776
	ds_read_b128 v[42:45], v37 offset:11792
	ds_read_b128 v[82:85], v37 offset:12048
	ds_read_b128 v[86:89], v37 offset:12032
	v_add_f32_e32 v24, v96, v24
	v_add_f32_e32 v92, v24, v25
	v_add_f32_e32 v24, v20, v21
	s_waitcnt lgkmcnt(2)
	v_mov_b32_e32 v20, v45
	s_waitcnt lgkmcnt(1)
	v_mov_b32_e32 v21, v85
	v_pk_mul_f32 v[20:21], v[22:23], v[20:21]
	s_waitcnt lgkmcnt(0)
	v_mov_b32_e32 v25, v86
	v_add_f32_e32 v20, v24, v20
	v_mov_b32_e32 v24, v38
	v_pk_mul_f32 v[24:25], v[22:23], v[24:25]
	v_mov_b32_e32 v86, v39
	v_add_f32_e32 v24, v81, v24
	v_add_f32_e32 v81, v24, v25
	v_mov_b32_e32 v24, v42
	v_mov_b32_e32 v25, v82
	v_pk_mul_f32 v[24:25], v[22:23], v[24:25]
	v_mov_b32_e32 v82, v43
	v_add_f32_e32 v24, v97, v24
	v_add_f32_e32 v93, v25, v24
	v_pk_mul_f32 v[24:25], v[22:23], v[86:87]
	v_mov_b32_e32 v45, v84
	v_add_f32_e32 v24, v90, v24
	v_add_f32_e32 v90, v24, v25
	v_pk_mul_f32 v[24:25], v[22:23], v[82:83]
	v_add_f32_e32 v82, v21, v20
	v_add_f32_e32 v24, v91, v24
	v_add_f32_e32 v91, v25, v24
	v_mov_b32_e32 v24, v40
	v_mov_b32_e32 v25, v88
	v_pk_mul_f32 v[24:25], v[22:23], v[24:25]
	v_mov_b32_e32 v88, v41
	v_add_f32_e32 v24, v94, v24
	v_add_f32_e32 v94, v24, v25
	v_pk_mul_f32 v[24:25], v[22:23], v[44:45]
	v_pk_mul_f32 v[22:23], v[22:23], v[88:89]
	v_add_f32_e32 v24, v95, v24
	v_add_f32_e32 v22, v92, v22
	v_add_f32_e32 v88, v22, v23
	ds_read_b128 v[20:23], v37 offset:12304
	ds_read_b128 v[38:41], v37 offset:12288
	ds_read_b128 v[42:45], v37 offset:12560
	v_add_f32_e32 v95, v25, v24
	s_waitcnt lgkmcnt(2)
	v_mov_b32_e32 v24, v23
	s_waitcnt lgkmcnt(1)
	v_mov_b32_e32 v86, v38
	s_waitcnt lgkmcnt(0)
	v_mov_b32_e32 v25, v45
	v_pk_mul_f32 v[24:25], v[18:19], v[24:25]
	s_nop 0
	v_add_f32_e32 v24, v82, v24
	ds_read_b128 v[82:85], v37 offset:12544
	s_waitcnt lgkmcnt(0)
	v_mov_b32_e32 v87, v82
	v_pk_mul_f32 v[86:87], v[18:19], v[86:87]
	v_mov_b32_e32 v82, v39
	v_add_f32_e32 v23, v81, v86
	v_add_f32_e32 v45, v23, v87
	v_mov_b32_e32 v86, v20
	v_mov_b32_e32 v87, v42
	v_pk_mul_f32 v[86:87], v[18:19], v[86:87]
	v_pk_mul_f32 v[38:39], v[18:19], v[82:83]
	v_add_f32_e32 v20, v93, v86
	v_add_f32_e32 v81, v20, v87
	v_add_f32_e32 v20, v90, v38
	v_mov_b32_e32 v42, v21
	v_add_f32_e32 v38, v20, v39
	v_pk_mul_f32 v[20:21], v[18:19], v[42:43]
	v_mov_b32_e32 v23, v44
	v_add_f32_e32 v20, v91, v20
	v_add_f32_e32 v39, v20, v21
	v_mov_b32_e32 v20, v40
	v_mov_b32_e32 v21, v84
	v_pk_mul_f32 v[20:21], v[18:19], v[20:21]
	v_mov_b32_e32 v84, v41
	v_add_f32_e32 v20, v94, v20
	v_add_f32_e32 v40, v20, v21
	v_pk_mul_f32 v[20:21], v[18:19], v[22:23]
	v_pk_mul_f32 v[18:19], v[18:19], v[84:85]
	v_add_f32_e32 v20, v95, v20
	v_add_f32_e32 v18, v88, v18
	v_add_f32_e32 v23, v20, v21
	v_add_f32_e32 v21, v18, v19
	v_mul_f32_e32 v18, 0xbfb8aa3b, v45
	v_exp_f32_e32 v18, v18
	v_add_f32_e32 v22, v24, v25
	v_mul_f32_e32 v21, 0xbfb8aa3b, v21
	v_exp_f32_e32 v21, v21
	v_add_f32_e32 v18, 1.0, v18
	v_cmp_gt_f32_e32 vcc, s93, v18
	v_mul_f32_e32 v23, 0xbfb8aa3b, v23
	v_add_f32_e32 v21, 1.0, v21
	v_cndmask_b32_e64 v19, 0, 32, vcc
	v_ldexp_f32 v18, v18, v19
	v_log_f32_e32 v18, v18
	v_exp_f32_e32 v23, v23
	v_mul_f32_e32 v22, 0xbfb8aa3b, v22
	v_exp_f32_e32 v22, v22
	v_mul_f32_e32 v19, 0x3f317217, v18
	v_fma_f32 v19, v18, s62, -v19
	v_fmac_f32_e32 v19, 0x3377d1cf, v18
	v_fmac_f32_e32 v19, 0x3f317217, v18
	v_cmp_lt_f32_e64 s[14:15], |v18|, s63
	v_add_f32_e32 v23, 1.0, v23
	v_add_f32_e32 v22, 1.0, v22
	v_cndmask_b32_e64 v18, v18, v19, s[14:15]
	v_cndmask_b32_e32 v19, 0, v243, vcc
	v_sub_f32_e32 v18, v18, v19
	v_mul_f32_e32 v19, 0xbfb8aa3b, v38
	v_exp_f32_e32 v19, v19
	s_nop 0
	v_add_f32_e32 v19, 1.0, v19
	v_cmp_gt_f32_e32 vcc, s93, v19
	s_nop 1
	v_cndmask_b32_e64 v20, 0, 32, vcc
	v_ldexp_f32 v19, v19, v20
	v_log_f32_e32 v19, v19
	s_nop 0
	v_mul_f32_e32 v20, 0x3f317217, v19
	v_fma_f32 v20, v19, s62, -v20
	v_fmac_f32_e32 v20, 0x3377d1cf, v19
	v_fmac_f32_e32 v20, 0x3f317217, v19
	v_cmp_lt_f32_e64 s[14:15], |v19|, s63
	s_nop 1
	v_cndmask_b32_e64 v19, v19, v20, s[14:15]
	v_cndmask_b32_e32 v20, 0, v243, vcc
	v_sub_f32_e32 v19, v19, v20
	v_mul_f32_e32 v20, 0xbfb8aa3b, v40
	v_exp_f32_e32 v20, v20
	v_pk_mul_f32 v[18:19], v[18:19], s[76:77] op_sel_hi:[1,0]
	v_add_f32_e32 v20, 1.0, v20
	v_cmp_gt_f32_e32 vcc, s93, v20
	v_cvt_pk_bf16_f32 v18, v18, v19
	s_nop 0
	v_cndmask_b32_e64 v24, 0, 32, vcc
	v_ldexp_f32 v20, v20, v24
	v_log_f32_e32 v20, v20
	s_nop 0
	v_mul_f32_e32 v24, 0x3f317217, v20
	v_fma_f32 v24, v20, s62, -v24
	v_fmac_f32_e32 v24, 0x3377d1cf, v20
	v_fmac_f32_e32 v24, 0x3f317217, v20
	v_cmp_lt_f32_e64 s[14:15], |v20|, s63
	s_nop 1
	v_cndmask_b32_e64 v20, v20, v24, s[14:15]
	v_cndmask_b32_e32 v24, 0, v243, vcc
	v_cmp_gt_f32_e32 vcc, s93, v21
	v_sub_f32_e32 v20, v20, v24
	s_nop 0
	v_cndmask_b32_e64 v24, 0, 32, vcc
	v_ldexp_f32 v21, v21, v24
	v_log_f32_e32 v21, v21
	s_nop 0
	v_mul_f32_e32 v24, 0x3f317217, v21
	v_fma_f32 v24, v21, s62, -v24
	v_fmac_f32_e32 v24, 0x3377d1cf, v21
	v_fmac_f32_e32 v24, 0x3f317217, v21
	v_cmp_lt_f32_e64 s[14:15], |v21|, s63
	s_nop 1
	v_cndmask_b32_e64 v21, v21, v24, s[14:15]
	v_cndmask_b32_e32 v24, 0, v243, vcc
	v_sub_f32_e32 v21, v21, v24
	v_mul_f32_e32 v24, 0xbfb8aa3b, v81
	v_exp_f32_e32 v24, v24
	v_pk_mul_f32 v[20:21], v[20:21], s[76:77] op_sel_hi:[1,0]
	v_add_f32_e32 v24, 1.0, v24
	v_cmp_gt_f32_e32 vcc, s93, v24
	v_cvt_pk_bf16_f32 v19, v20, v21
	s_nop 0
	v_cndmask_b32_e64 v25, 0, 32, vcc
	v_ldexp_f32 v24, v24, v25
	v_log_f32_e32 v24, v24
	s_nop 0
	v_mul_f32_e32 v25, 0x3f317217, v24
	v_fma_f32 v25, v24, s62, -v25
	v_fmac_f32_e32 v25, 0x3377d1cf, v24
	v_fmac_f32_e32 v25, 0x3f317217, v24
	v_cmp_lt_f32_e64 s[14:15], |v24|, s63
	s_nop 1
	v_cndmask_b32_e64 v24, v24, v25, s[14:15]
	v_cndmask_b32_e32 v25, 0, v243, vcc
	v_sub_f32_e32 v24, v24, v25
	v_mul_f32_e32 v25, 0xbfb8aa3b, v39
	v_exp_f32_e32 v25, v25
	s_nop 0
	v_add_f32_e32 v25, 1.0, v25
	v_cmp_gt_f32_e32 vcc, s93, v25
	s_nop 1
	v_cndmask_b32_e64 v38, 0, 32, vcc
	v_ldexp_f32 v25, v25, v38
	v_log_f32_e32 v25, v25
	s_nop 0
	v_mul_f32_e32 v38, 0x3f317217, v25
	v_fma_f32 v38, v25, s62, -v38
	v_fmac_f32_e32 v38, 0x3377d1cf, v25
	v_fmac_f32_e32 v38, 0x3f317217, v25
	v_cmp_lt_f32_e64 s[14:15], |v25|, s63
	s_nop 1
	v_cndmask_b32_e64 v25, v25, v38, s[14:15]
	v_cndmask_b32_e32 v38, 0, v243, vcc
	v_cmp_gt_f32_e32 vcc, s93, v23
	v_sub_f32_e32 v25, v25, v38
	v_pk_mul_f32 v[24:25], v[24:25], s[76:77] op_sel_hi:[1,0]
	v_cndmask_b32_e64 v38, 0, 32, vcc
	v_ldexp_f32 v23, v23, v38
	v_log_f32_e32 v23, v23
	v_cvt_pk_bf16_f32 v20, v24, v25
	v_lshlrev_b32_e32 v24, 16, v18
	v_and_b32_e32 v25, 0xffff0000, v18
	v_mul_f32_e32 v38, 0x3f317217, v23
	v_fma_f32 v38, v23, s62, -v38
	v_fmac_f32_e32 v38, 0x3377d1cf, v23
	v_fmac_f32_e32 v38, 0x3f317217, v23
	v_cmp_lt_f32_e64 s[14:15], |v23|, s63
	v_lshlrev_b32_e32 v40, 16, v20
	v_and_b32_e32 v41, 0xffff0000, v20
	v_cndmask_b32_e64 v23, v23, v38, s[14:15]
	v_cndmask_b32_e32 v38, 0, v243, vcc
	v_cmp_gt_f32_e32 vcc, s93, v22
	v_sub_f32_e32 v38, v23, v38
	s_nop 0
	v_cndmask_b32_e64 v23, 0, 32, vcc
	v_ldexp_f32 v22, v22, v23
	v_log_f32_e32 v22, v22
	s_nop 0
	v_mul_f32_e32 v23, 0x3f317217, v22
	v_fma_f32 v23, v22, s62, -v23
	v_fmac_f32_e32 v23, 0x3377d1cf, v22
	v_fmac_f32_e32 v23, 0x3f317217, v22
	v_cmp_lt_f32_e64 s[14:15], |v22|, s63
	s_nop 1
	v_cndmask_b32_e64 v22, v22, v23, s[14:15]
	v_cndmask_b32_e32 v23, 0, v243, vcc
	v_sub_f32_e32 v39, v22, v23
	v_pk_mul_f32 v[22:23], v[38:39], s[76:77] op_sel_hi:[1,0]
	v_lshlrev_b32_e32 v38, 16, v19
	v_cvt_pk_bf16_f32 v21, v22, v23
	v_lshl_add_u64 v[22:23], v[26:27], 0, s[0:1]
	global_store_dwordx4 v[22:23], v[18:21], off
	v_and_b32_e32 v39, 0xffff0000, v19
	v_lshlrev_b32_e32 v42, 16, v21
	v_add_f32_dpp v18, v24, v24 row_shr:1 row_mask:0xf bank_mask:0xf bound_ctrl:1
	v_mov_b32_e32 v19, v69
	v_and_b32_e32 v43, 0xffff0000, v21
	v_add_f32_dpp v18, v18, v18 row_shr:2 row_mask:0xf bank_mask:0xf bound_ctrl:1
	s_add_i32 s0, s26, 1
	s_ashr_i32 s1, s0, 31
	v_add_f32_dpp v18, v18, v18 row_shr:4 row_mask:0xf bank_mask:0xf bound_ctrl:1
	s_lshl_b64 s[0:1], s[0:1], 13
	s_nop 0
	v_add_f32_dpp v18, v18, v18 row_shr:8 row_mask:0xf bank_mask:0xf bound_ctrl:1
	s_nop 1
	v_mov_b32_dpp v19, v18 row_bcast:15 row_mask:0xa bank_mask:0xf bound_ctrl:1
	v_add_f32_e32 v18, v18, v19
	v_mov_b32_e32 v19, v69
	s_nop 1
	v_mov_b32_dpp v19, v18 row_bcast:31 row_mask:0xc bank_mask:0xf bound_ctrl:1
	v_add_f32_e32 v88, v18, v19
	v_add_f32_dpp v18, v25, v25 row_shr:1 row_mask:0xf bank_mask:0xf bound_ctrl:1
	v_mov_b32_e32 v19, v69
	v_readlane_b32 s27, v88, 63
	v_add_f32_dpp v18, v18, v18 row_shr:2 row_mask:0xf bank_mask:0xf bound_ctrl:1
	s_nop 1
	v_add_f32_dpp v18, v18, v18 row_shr:4 row_mask:0xf bank_mask:0xf bound_ctrl:1
	s_nop 1
	v_add_f32_dpp v18, v18, v18 row_shr:8 row_mask:0xf bank_mask:0xf bound_ctrl:1
	s_nop 1
	v_mov_b32_dpp v19, v18 row_bcast:15 row_mask:0xa bank_mask:0xf bound_ctrl:1
	v_add_f32_e32 v18, v18, v19
	v_mov_b32_e32 v19, v69
	s_nop 1
	v_mov_b32_dpp v19, v18 row_bcast:31 row_mask:0xc bank_mask:0xf bound_ctrl:1
	v_add_f32_e32 v87, v18, v19
	v_add_f32_dpp v18, v38, v38 row_shr:1 row_mask:0xf bank_mask:0xf bound_ctrl:1
	v_mov_b32_e32 v19, v69
	v_add_u32_e32 v38, 0x1100, v57
	v_add_f32_dpp v18, v18, v18 row_shr:2 row_mask:0xf bank_mask:0xf bound_ctrl:1
	v_readlane_b32 s48, v87, 63
	s_nop 0
	v_add_f32_dpp v18, v18, v18 row_shr:4 row_mask:0xf bank_mask:0xf bound_ctrl:1
	s_nop 1
	v_add_f32_dpp v18, v18, v18 row_shr:8 row_mask:0xf bank_mask:0xf bound_ctrl:1
	s_nop 1
	v_mov_b32_dpp v19, v18 row_bcast:15 row_mask:0xa bank_mask:0xf bound_ctrl:1
	v_add_f32_e32 v18, v18, v19
	v_mov_b32_e32 v19, v69
	s_nop 1
	v_mov_b32_dpp v19, v18 row_bcast:31 row_mask:0xc bank_mask:0xf bound_ctrl:1
	v_add_f32_e32 v86, v18, v19
	v_add_f32_dpp v18, v39, v39 row_shr:1 row_mask:0xf bank_mask:0xf bound_ctrl:1
	v_mov_b32_e32 v19, v69
	v_readlane_b32 s50, v86, 63
	v_add_f32_dpp v18, v18, v18 row_shr:2 row_mask:0xf bank_mask:0xf bound_ctrl:1
	s_nop 1
	v_add_f32_dpp v18, v18, v18 row_shr:4 row_mask:0xf bank_mask:0xf bound_ctrl:1
	s_nop 1
	v_add_f32_dpp v18, v18, v18 row_shr:8 row_mask:0xf bank_mask:0xf bound_ctrl:1
	s_nop 1
	v_mov_b32_dpp v19, v18 row_bcast:15 row_mask:0xa bank_mask:0xf bound_ctrl:1
	v_add_f32_e32 v18, v18, v19
	v_mov_b32_e32 v19, v69
	s_nop 1
	v_mov_b32_dpp v19, v18 row_bcast:31 row_mask:0xc bank_mask:0xf bound_ctrl:1
	v_add_f32_e32 v85, v18, v19
	v_add_f32_dpp v18, v40, v40 row_shr:1 row_mask:0xf bank_mask:0xf bound_ctrl:1
	v_mov_b32_e32 v19, v69
	v_add_u32_e32 v40, 0x1108, v57
	v_add_f32_dpp v18, v18, v18 row_shr:2 row_mask:0xf bank_mask:0xf bound_ctrl:1
	v_readlane_b32 s56, v85, 63
	s_nop 0
	v_add_f32_dpp v18, v18, v18 row_shr:4 row_mask:0xf bank_mask:0xf bound_ctrl:1
	s_nop 1
	v_add_f32_dpp v18, v18, v18 row_shr:8 row_mask:0xf bank_mask:0xf bound_ctrl:1
	s_nop 1
	v_mov_b32_dpp v19, v18 row_bcast:15 row_mask:0xa bank_mask:0xf bound_ctrl:1
	v_add_f32_e32 v18, v18, v19
	v_mov_b32_e32 v19, v69
	s_nop 1
	v_mov_b32_dpp v19, v18 row_bcast:31 row_mask:0xc bank_mask:0xf bound_ctrl:1
	v_add_f32_e32 v84, v18, v19
	v_add_f32_dpp v18, v41, v41 row_shr:1 row_mask:0xf bank_mask:0xf bound_ctrl:1
	v_mov_b32_e32 v19, v69
	v_readlane_b32 s49, v84, 63
	v_add_f32_dpp v18, v18, v18 row_shr:2 row_mask:0xf bank_mask:0xf bound_ctrl:1
	s_nop 1
	v_add_f32_dpp v18, v18, v18 row_shr:4 row_mask:0xf bank_mask:0xf bound_ctrl:1
	s_nop 1
	v_add_f32_dpp v18, v18, v18 row_shr:8 row_mask:0xf bank_mask:0xf bound_ctrl:1
	s_nop 1
	v_mov_b32_dpp v19, v18 row_bcast:15 row_mask:0xa bank_mask:0xf bound_ctrl:1
	v_add_f32_e32 v18, v18, v19
	v_mov_b32_e32 v19, v69
	s_nop 1
	v_mov_b32_dpp v19, v18 row_bcast:31 row_mask:0xc bank_mask:0xf bound_ctrl:1
	v_add_f32_e32 v83, v18, v19
	v_add_f32_dpp v18, v42, v42 row_shr:1 row_mask:0xf bank_mask:0xf bound_ctrl:1
	v_mov_b32_e32 v19, v69
	v_readlane_b32 s51, v83, 63
	v_add_f32_dpp v18, v18, v18 row_shr:2 row_mask:0xf bank_mask:0xf bound_ctrl:1
	s_nop 1
	v_add_f32_dpp v18, v18, v18 row_shr:4 row_mask:0xf bank_mask:0xf bound_ctrl:1
	s_nop 1
	v_add_f32_dpp v18, v18, v18 row_shr:8 row_mask:0xf bank_mask:0xf bound_ctrl:1
	s_nop 1
	v_mov_b32_dpp v19, v18 row_bcast:15 row_mask:0xa bank_mask:0xf bound_ctrl:1
	v_add_f32_e32 v18, v18, v19
	v_mov_b32_e32 v19, v69
	s_nop 1
	v_mov_b32_dpp v19, v18 row_bcast:31 row_mask:0xc bank_mask:0xf bound_ctrl:1
	v_add_f32_e32 v82, v18, v19
	v_add_f32_dpp v18, v43, v43 row_shr:1 row_mask:0xf bank_mask:0xf bound_ctrl:1
	v_mov_b32_e32 v19, v69
	v_readlane_b32 s57, v82, 63
	v_add_f32_dpp v18, v18, v18 row_shr:2 row_mask:0xf bank_mask:0xf bound_ctrl:1
	s_nop 1
	v_add_f32_dpp v18, v18, v18 row_shr:4 row_mask:0xf bank_mask:0xf bound_ctrl:1
	s_nop 1
	v_add_f32_dpp v18, v18, v18 row_shr:8 row_mask:0xf bank_mask:0xf bound_ctrl:1
	s_nop 1
	v_mov_b32_dpp v19, v18 row_bcast:15 row_mask:0xa bank_mask:0xf bound_ctrl:1
	v_add_f32_e32 v18, v18, v19
	v_mov_b32_e32 v19, v69
	s_nop 1
	v_mov_b32_dpp v19, v18 row_bcast:31 row_mask:0xc bank_mask:0xf bound_ctrl:1
	v_add_f32_e32 v81, v18, v19
	ds_read_b128 v[90:93], v37 offset:12800
	ds_read_b128 v[94:97], v37 offset:12816
	ds_read_b128 v[22:25], v37 offset:17168
	ds_read_b128 v[18:21], v37 offset:17152
	ds_read2_b32 v[38:39], v38 offset1:1
	ds_read2_b32 v[44:45], v40 offset1:1
	v_add_u32_e32 v40, 0x1110, v57
	ds_read2_b32 v[42:43], v40 offset1:1
	v_add_u32_e32 v40, 0x1118, v57
	ds_read2_b32 v[40:41], v40 offset1:1
	s_waitcnt lgkmcnt(3)
	v_fma_f32 v89, v90, v38, v18
	v_fma_f32 v104, v94, v38, v22
	v_fma_f32 v105, v91, v38, v19
	v_fma_f32 v106, v95, v38, v23
	v_fma_f32 v20, v92, v38, v20
	v_fma_f32 v107, v96, v38, v24
	v_fmac_f32_e32 v21, v93, v38
	v_fmac_f32_e32 v25, v97, v38
	ds_read_b128 v[90:93], v37 offset:13072
	ds_read_b128 v[94:97], v37 offset:13056
	v_add_u32_e32 v18, 0x1138, v57
	v_add_u32_e32 v22, 0x1130, v57
	v_add_u32_e32 v24, 0x1128, v57
	s_waitcnt lgkmcnt(1)
	v_fmac_f32_e32 v104, v39, v90
	s_waitcnt lgkmcnt(0)
	v_fmac_f32_e32 v89, v39, v94
	v_fmac_f32_e32 v105, v39, v95
	v_fmac_f32_e32 v106, v39, v91
	v_fmac_f32_e32 v20, v39, v96
	v_fmac_f32_e32 v107, v39, v92
	v_fmac_f32_e32 v21, v39, v97
	v_fmac_f32_e32 v25, v39, v93
	ds_read_b128 v[90:93], v37 offset:13328
	ds_read_b128 v[94:97], v37 offset:13312
	v_readlane_b32 s70, v81, 63
	s_waitcnt lgkmcnt(1)
	v_fmac_f32_e32 v104, v44, v90
	s_waitcnt lgkmcnt(0)
	v_fmac_f32_e32 v89, v44, v94
	v_fmac_f32_e32 v105, v44, v95
	v_fmac_f32_e32 v106, v44, v91
	v_fmac_f32_e32 v20, v44, v96
	v_fmac_f32_e32 v107, v44, v92
	v_fmac_f32_e32 v21, v44, v97
	v_fmac_f32_e32 v25, v44, v93
	ds_read_b128 v[90:93], v37 offset:13584
	ds_read_b128 v[94:97], v37 offset:13568
	ds_read2_b32 v[18:19], v18 offset1:1
	ds_read2_b32 v[22:23], v22 offset1:1
	ds_read2_b32 v[38:39], v24 offset1:1
	v_add_u32_e32 v24, 0x1120, v57
	s_waitcnt lgkmcnt(3)
	v_fmac_f32_e32 v89, v45, v94
	v_fmac_f32_e32 v104, v45, v90
	v_fmac_f32_e32 v105, v45, v95
	v_fmac_f32_e32 v106, v45, v91
	v_fmac_f32_e32 v20, v45, v96
	v_fmac_f32_e32 v107, v45, v92
	v_fmac_f32_e32 v21, v45, v97
	v_fmac_f32_e32 v25, v45, v93
	ds_read2_b32 v[44:45], v24 offset1:1
	ds_read_b128 v[90:93], v37 offset:13824
	ds_read_b128 v[94:97], v37 offset:13840
	s_waitcnt lgkmcnt(1)
	v_fmac_f32_e32 v89, v42, v90
	s_waitcnt lgkmcnt(0)
	v_fmac_f32_e32 v104, v42, v94
	v_fmac_f32_e32 v105, v42, v91
	v_fmac_f32_e32 v106, v42, v95
	v_fmac_f32_e32 v20, v42, v92
	v_fmac_f32_e32 v107, v42, v96
	v_fmac_f32_e32 v21, v42, v93
	v_fmac_f32_e32 v25, v42, v97
	ds_read_b128 v[90:93], v37 offset:14096
	ds_read_b128 v[94:97], v37 offset:14080
	s_waitcnt lgkmcnt(1)
	v_fmac_f32_e32 v104, v43, v90
	s_waitcnt lgkmcnt(0)
	v_fmac_f32_e32 v89, v43, v94
	v_fmac_f32_e32 v105, v43, v95
	v_fmac_f32_e32 v106, v43, v91
	v_fmac_f32_e32 v20, v43, v96
	v_fmac_f32_e32 v107, v43, v92
	v_fmac_f32_e32 v21, v43, v97
	v_fmac_f32_e32 v25, v43, v93
	ds_read_b128 v[90:93], v37 offset:14352
	ds_read_b128 v[94:97], v37 offset:14336
	s_waitcnt lgkmcnt(1)
	v_fmac_f32_e32 v104, v40, v90
	s_waitcnt lgkmcnt(0)
	v_fmac_f32_e32 v89, v40, v94
	v_fmac_f32_e32 v105, v40, v95
	v_fmac_f32_e32 v106, v40, v91
	v_fmac_f32_e32 v20, v40, v96
	v_fmac_f32_e32 v107, v40, v92
	v_fmac_f32_e32 v21, v40, v97
	v_fmac_f32_e32 v25, v40, v93
	ds_read_b128 v[90:93], v37 offset:14608
	ds_read_b128 v[94:97], v37 offset:14592
	s_waitcnt lgkmcnt(1)
	v_fmac_f32_e32 v104, v41, v90
	s_waitcnt lgkmcnt(0)
	v_fmac_f32_e32 v89, v41, v94
	v_fmac_f32_e32 v105, v41, v95
	v_fmac_f32_e32 v106, v41, v91
	v_fmac_f32_e32 v20, v41, v96
	v_fmac_f32_e32 v107, v41, v92
	v_fmac_f32_e32 v21, v41, v97
	v_fmac_f32_e32 v25, v41, v93
	ds_read_b128 v[40:43], v37 offset:14848
	ds_read_b128 v[90:93], v37 offset:14864
	ds_read_b128 v[94:97], v37 offset:15120
	s_waitcnt lgkmcnt(2)
	v_mov_b32_e32 v24, v40
	s_waitcnt lgkmcnt(1)
	v_mov_b32_e32 v98, v93
	s_waitcnt lgkmcnt(0)
	v_mov_b32_e32 v99, v97
	v_pk_mul_f32 v[102:103], v[44:45], v[98:99]
	ds_read_b128 v[98:101], v37 offset:15104
	v_add_f32_e32 v97, v25, v102
	v_mov_b32_e32 v93, v96
	s_waitcnt lgkmcnt(0)
	v_mov_b32_e32 v25, v98
	v_pk_mul_f32 v[24:25], v[44:45], v[24:25]
	v_mov_b32_e32 v98, v41
	v_add_f32_e32 v24, v89, v24
	v_add_f32_e32 v89, v24, v25
	v_mov_b32_e32 v24, v90
	v_mov_b32_e32 v25, v94
	v_pk_mul_f32 v[24:25], v[44:45], v[24:25]
	v_mov_b32_e32 v94, v91
	v_add_f32_e32 v24, v104, v24
	v_add_f32_e32 v102, v25, v24
	v_pk_mul_f32 v[24:25], v[44:45], v[98:99]
	s_nop 0
	v_add_f32_e32 v24, v105, v24
	v_add_f32_e32 v104, v24, v25
	v_pk_mul_f32 v[24:25], v[44:45], v[94:95]
	s_nop 0
	v_add_f32_e32 v24, v106, v24
	v_add_f32_e32 v105, v25, v24
	v_mov_b32_e32 v24, v42
	v_mov_b32_e32 v25, v100
	v_pk_mul_f32 v[24:25], v[44:45], v[24:25]
	v_mov_b32_e32 v100, v43
	v_add_f32_e32 v20, v20, v24
	v_add_f32_e32 v106, v20, v25
	v_pk_mul_f32 v[24:25], v[44:45], v[92:93]
	s_nop 0
	v_add_f32_e32 v20, v107, v24
	v_add_f32_e32 v107, v25, v20
	v_pk_mul_f32 v[24:25], v[44:45], v[100:101]
	s_nop 0
	v_add_f32_e32 v20, v21, v24
	v_add_f32_e32 v24, v103, v97
	ds_read_b128 v[40:43], v37 offset:15376
	ds_read_b128 v[90:93], v37 offset:15360
	ds_read_b128 v[94:97], v37 offset:15632
	ds_read_b128 v[98:101], v37 offset:15616
	v_add_f32_e32 v44, v20, v25
	s_waitcnt lgkmcnt(3)
	v_mov_b32_e32 v20, v43
	s_waitcnt lgkmcnt(1)
	v_mov_b32_e32 v21, v97
	v_pk_mul_f32 v[20:21], v[38:39], v[20:21]
	s_waitcnt lgkmcnt(0)
	v_mov_b32_e32 v25, v98
	v_add_f32_e32 v20, v24, v20
	v_mov_b32_e32 v24, v90
	v_pk_mul_f32 v[24:25], v[38:39], v[24:25]
	v_mov_b32_e32 v98, v91
	v_add_f32_e32 v24, v89, v24
	v_add_f32_e32 v89, v24, v25
	v_mov_b32_e32 v24, v40
	v_mov_b32_e32 v25, v94
	v_pk_mul_f32 v[24:25], v[38:39], v[24:25]
	v_mov_b32_e32 v94, v41
	v_add_f32_e32 v24, v102, v24
	v_add_f32_e32 v102, v24, v25
	v_pk_mul_f32 v[24:25], v[38:39], v[98:99]
	v_mov_b32_e32 v43, v96
	v_add_f32_e32 v24, v104, v24
	v_add_f32_e32 v98, v24, v25
	v_pk_mul_f32 v[24:25], v[38:39], v[94:95]
	s_nop 0
	v_add_f32_e32 v24, v105, v24
	v_add_f32_e32 v99, v24, v25
	v_mov_b32_e32 v24, v92
	v_mov_b32_e32 v25, v100
	v_pk_mul_f32 v[24:25], v[38:39], v[24:25]
	v_mov_b32_e32 v100, v93
	v_add_f32_e32 v24, v106, v24
	v_add_f32_e32 v103, v24, v25
	v_pk_mul_f32 v[24:25], v[38:39], v[42:43]
	s_nop 0
	v_add_f32_e32 v24, v107, v24
	v_add_f32_e32 v104, v24, v25
	v_pk_mul_f32 v[24:25], v[38:39], v[100:101]
	s_nop 0
	v_add_f32_e32 v24, v44, v24
	ds_read_b128 v[38:41], v37 offset:15872
	ds_read_b128 v[42:45], v37 offset:15888
	ds_read_b128 v[90:93], v37 offset:16144
	ds_read_b128 v[94:97], v37 offset:16128
	v_add_f32_e32 v100, v24, v25
	v_add_f32_e32 v24, v20, v21
	s_waitcnt lgkmcnt(2)
	v_mov_b32_e32 v20, v45
	s_waitcnt lgkmcnt(1)
	v_mov_b32_e32 v21, v93
	v_pk_mul_f32 v[20:21], v[22:23], v[20:21]
	s_waitcnt lgkmcnt(0)
	v_mov_b32_e32 v25, v94
	v_add_f32_e32 v20, v24, v20
	v_mov_b32_e32 v24, v38
	v_pk_mul_f32 v[24:25], v[22:23], v[24:25]
	v_mov_b32_e32 v94, v39
	v_add_f32_e32 v24, v89, v24
	v_add_f32_e32 v89, v24, v25
	v_mov_b32_e32 v24, v42
	v_mov_b32_e32 v25, v90
	v_pk_mul_f32 v[24:25], v[22:23], v[24:25]
	v_mov_b32_e32 v90, v43
	v_add_f32_e32 v24, v102, v24
	v_add_f32_e32 v101, v25, v24
	v_pk_mul_f32 v[24:25], v[22:23], v[94:95]
	v_mov_b32_e32 v45, v92
	v_add_f32_e32 v24, v98, v24
	v_add_f32_e32 v98, v24, v25
	v_pk_mul_f32 v[24:25], v[22:23], v[90:91]
	v_add_f32_e32 v90, v21, v20
	v_add_f32_e32 v24, v99, v24
	v_add_f32_e32 v99, v25, v24
	v_mov_b32_e32 v24, v40
	v_mov_b32_e32 v25, v96
	v_pk_mul_f32 v[24:25], v[22:23], v[24:25]
	v_mov_b32_e32 v96, v41
	v_add_f32_e32 v24, v103, v24
	v_add_f32_e32 v102, v24, v25
	v_pk_mul_f32 v[24:25], v[22:23], v[44:45]
	v_pk_mul_f32 v[22:23], v[22:23], v[96:97]
	v_add_f32_e32 v24, v104, v24
	v_add_f32_e32 v22, v100, v22
	v_add_f32_e32 v96, v22, v23
	ds_read_b128 v[20:23], v37 offset:16400
	ds_read_b128 v[38:41], v37 offset:16384
	ds_read_b128 v[42:45], v37 offset:16656
	v_add_f32_e32 v103, v25, v24
	s_waitcnt lgkmcnt(2)
	v_mov_b32_e32 v24, v23
	s_waitcnt lgkmcnt(1)
	v_mov_b32_e32 v94, v38
	s_waitcnt lgkmcnt(0)
	v_mov_b32_e32 v25, v45
	v_pk_mul_f32 v[24:25], v[18:19], v[24:25]
	s_nop 0
	v_add_f32_e32 v24, v90, v24
	ds_read_b128 v[90:93], v37 offset:16640
	s_waitcnt lgkmcnt(0)
	v_mov_b32_e32 v95, v90
	v_pk_mul_f32 v[94:95], v[18:19], v[94:95]
	v_mov_b32_e32 v90, v39
	v_add_f32_e32 v23, v89, v94
	v_add_f32_e32 v37, v23, v95
	v_mov_b32_e32 v94, v20
	v_mov_b32_e32 v95, v42
	v_pk_mul_f32 v[94:95], v[18:19], v[94:95]
	v_pk_mul_f32 v[38:39], v[18:19], v[90:91]
	v_add_f32_e32 v20, v101, v94
	v_add_f32_e32 v45, v20, v95
	v_add_f32_e32 v20, v98, v38
	v_mov_b32_e32 v42, v21
	v_add_f32_e32 v38, v20, v39
	v_pk_mul_f32 v[20:21], v[18:19], v[42:43]
	v_mov_b32_e32 v23, v44
	v_add_f32_e32 v20, v99, v20
	v_add_f32_e32 v39, v20, v21
	v_mov_b32_e32 v20, v40
	v_mov_b32_e32 v21, v92
	v_pk_mul_f32 v[20:21], v[18:19], v[20:21]
	v_mov_b32_e32 v92, v41
	v_add_f32_e32 v20, v102, v20
	v_add_f32_e32 v40, v20, v21
	v_pk_mul_f32 v[20:21], v[18:19], v[22:23]
	v_pk_mul_f32 v[18:19], v[18:19], v[92:93]
	v_add_f32_e32 v20, v103, v20
	v_add_f32_e32 v18, v96, v18
	v_add_f32_e32 v23, v20, v21
	v_add_f32_e32 v21, v18, v19
	v_mul_f32_e32 v18, 0xbfb8aa3b, v37
	v_exp_f32_e32 v18, v18
	v_add_f32_e32 v22, v24, v25
	v_mul_f32_e32 v21, 0xbfb8aa3b, v21
	v_exp_f32_e32 v21, v21
	v_add_f32_e32 v18, 1.0, v18
	v_cmp_gt_f32_e32 vcc, s93, v18
	v_mul_f32_e32 v23, 0xbfb8aa3b, v23
	v_add_f32_e32 v21, 1.0, v21
	v_cndmask_b32_e64 v19, 0, 32, vcc
	v_ldexp_f32 v18, v18, v19
	v_log_f32_e32 v18, v18
	v_exp_f32_e32 v23, v23
	v_mul_f32_e32 v22, 0xbfb8aa3b, v22
	v_exp_f32_e32 v22, v22
	v_mul_f32_e32 v19, 0x3f317217, v18
	v_fma_f32 v19, v18, s62, -v19
	v_fmac_f32_e32 v19, 0x3377d1cf, v18
	v_fmac_f32_e32 v19, 0x3f317217, v18
	v_cmp_lt_f32_e64 s[14:15], |v18|, s63
	v_add_f32_e32 v23, 1.0, v23
	v_add_f32_e32 v22, 1.0, v22
	v_cndmask_b32_e64 v18, v18, v19, s[14:15]
	v_cndmask_b32_e32 v19, 0, v243, vcc
	v_sub_f32_e32 v18, v18, v19
	v_mul_f32_e32 v19, 0xbfb8aa3b, v38
	v_exp_f32_e32 v19, v19
	s_nop 0
	v_add_f32_e32 v19, 1.0, v19
	v_cmp_gt_f32_e32 vcc, s93, v19
	s_nop 1
	v_cndmask_b32_e64 v20, 0, 32, vcc
	v_ldexp_f32 v19, v19, v20
	v_log_f32_e32 v19, v19
	s_nop 0
	v_mul_f32_e32 v20, 0x3f317217, v19
	v_fma_f32 v20, v19, s62, -v20
	v_fmac_f32_e32 v20, 0x3377d1cf, v19
	v_fmac_f32_e32 v20, 0x3f317217, v19
	v_cmp_lt_f32_e64 s[14:15], |v19|, s63
	s_nop 1
	v_cndmask_b32_e64 v19, v19, v20, s[14:15]
	v_cndmask_b32_e32 v20, 0, v243, vcc
	v_sub_f32_e32 v19, v19, v20
	v_mul_f32_e32 v20, 0xbfb8aa3b, v40
	v_exp_f32_e32 v20, v20
	v_pk_mul_f32 v[18:19], v[18:19], s[76:77] op_sel_hi:[1,0]
	v_add_f32_e32 v20, 1.0, v20
	v_cmp_gt_f32_e32 vcc, s93, v20
	v_cvt_pk_bf16_f32 v18, v18, v19
	s_nop 0
	v_cndmask_b32_e64 v24, 0, 32, vcc
	v_ldexp_f32 v20, v20, v24
	v_log_f32_e32 v20, v20
	s_nop 0
	v_mul_f32_e32 v24, 0x3f317217, v20
	v_fma_f32 v24, v20, s62, -v24
	v_fmac_f32_e32 v24, 0x3377d1cf, v20
	v_fmac_f32_e32 v24, 0x3f317217, v20
	v_cmp_lt_f32_e64 s[14:15], |v20|, s63
	s_nop 1
	v_cndmask_b32_e64 v20, v20, v24, s[14:15]
	v_cndmask_b32_e32 v24, 0, v243, vcc
	v_cmp_gt_f32_e32 vcc, s93, v21
	v_sub_f32_e32 v20, v20, v24
	s_nop 0
	v_cndmask_b32_e64 v24, 0, 32, vcc
	v_ldexp_f32 v21, v21, v24
	v_log_f32_e32 v21, v21
	s_nop 0
	v_mul_f32_e32 v24, 0x3f317217, v21
	v_fma_f32 v24, v21, s62, -v24
	v_fmac_f32_e32 v24, 0x3377d1cf, v21
	v_fmac_f32_e32 v24, 0x3f317217, v21
	v_cmp_lt_f32_e64 s[14:15], |v21|, s63
	s_nop 1
	v_cndmask_b32_e64 v21, v21, v24, s[14:15]
	v_cndmask_b32_e32 v24, 0, v243, vcc
	v_sub_f32_e32 v21, v21, v24
	v_mul_f32_e32 v24, 0xbfb8aa3b, v45
	v_exp_f32_e32 v24, v24
	v_pk_mul_f32 v[20:21], v[20:21], s[76:77] op_sel_hi:[1,0]
	v_sub_f32_e32 v45, s27, v88
	v_cvt_pk_bf16_f32 v19, v20, v21
	v_add_f32_e32 v24, 1.0, v24
	v_cmp_gt_f32_e32 vcc, s93, v24
	v_mul_f32_e32 v45, 0x3fb8aa3b, v45
	v_exp_f32_e32 v45, v45
	v_cndmask_b32_e64 v25, 0, 32, vcc
	v_ldexp_f32 v24, v24, v25
	v_log_f32_e32 v24, v24
	s_nop 0
	v_mul_f32_e32 v25, 0x3f317217, v24
	v_fma_f32 v25, v24, s62, -v25
	v_fmac_f32_e32 v25, 0x3377d1cf, v24
	v_fmac_f32_e32 v25, 0x3f317217, v24
	v_cmp_lt_f32_e64 s[14:15], |v24|, s63
	s_nop 1
	v_cndmask_b32_e64 v24, v24, v25, s[14:15]
	v_cndmask_b32_e32 v25, 0, v243, vcc
	v_sub_f32_e32 v24, v24, v25
	v_mul_f32_e32 v25, 0xbfb8aa3b, v39
	v_exp_f32_e32 v25, v25
	s_nop 0
	v_add_f32_e32 v25, 1.0, v25
	v_cmp_gt_f32_e32 vcc, s93, v25
	s_nop 1
	v_cndmask_b32_e64 v37, 0, 32, vcc
	v_ldexp_f32 v25, v25, v37
	v_log_f32_e32 v25, v25
	s_nop 0
	v_mul_f32_e32 v37, 0x3f317217, v25
	v_fma_f32 v37, v25, s62, -v37
	v_fmac_f32_e32 v37, 0x3377d1cf, v25
	v_fmac_f32_e32 v37, 0x3f317217, v25
	v_cmp_lt_f32_e64 s[14:15], |v25|, s63
	s_nop 1
	v_cndmask_b32_e64 v25, v25, v37, s[14:15]
	v_cndmask_b32_e32 v37, 0, v243, vcc
	v_cmp_gt_f32_e32 vcc, s93, v23
	v_sub_f32_e32 v25, v25, v37
	v_pk_mul_f32 v[24:25], v[24:25], s[76:77] op_sel_hi:[1,0]
	v_cndmask_b32_e64 v37, 0, 32, vcc
	v_ldexp_f32 v23, v23, v37
	v_log_f32_e32 v23, v23
	v_cvt_pk_bf16_f32 v20, v24, v25
	v_lshlrev_b32_e32 v24, 16, v18
	v_and_b32_e32 v25, 0xffff0000, v18
	v_mul_f32_e32 v37, 0x3f317217, v23
	v_fma_f32 v37, v23, s62, -v37
	v_fmac_f32_e32 v37, 0x3377d1cf, v23
	v_fmac_f32_e32 v37, 0x3f317217, v23
	v_cmp_lt_f32_e64 s[14:15], |v23|, s63
	v_and_b32_e32 v40, 0xffff0000, v20
	s_nop 0
	v_cndmask_b32_e64 v23, v23, v37, s[14:15]
	v_cndmask_b32_e32 v37, 0, v243, vcc
	v_cmp_gt_f32_e32 vcc, s93, v22
	v_sub_f32_e32 v38, v23, v37
	v_lshlrev_b32_e32 v37, 16, v19
	v_cndmask_b32_e64 v23, 0, 32, vcc
	v_ldexp_f32 v22, v22, v23
	v_log_f32_e32 v22, v22
	s_nop 0
	v_mul_f32_e32 v23, 0x3f317217, v22
	v_fma_f32 v23, v22, s62, -v23
	v_fmac_f32_e32 v23, 0x3377d1cf, v22
	v_fmac_f32_e32 v23, 0x3f317217, v22
	v_cmp_lt_f32_e64 s[14:15], |v22|, s63
	s_nop 1
	v_cndmask_b32_e64 v22, v22, v23, s[14:15]
	v_cndmask_b32_e32 v23, 0, v243, vcc
	v_sub_f32_e32 v39, v22, v23
	v_pk_mul_f32 v[22:23], v[38:39], s[76:77] op_sel_hi:[1,0]
	v_and_b32_e32 v38, 0xffff0000, v19
	v_cvt_pk_bf16_f32 v21, v22, v23
	v_lshl_add_u64 v[22:23], v[26:27], 0, s[0:1]
	global_store_dwordx4 v[22:23], v[18:21], off
	v_lshlrev_b32_e32 v39, 16, v20
	v_lshlrev_b32_e32 v41, 16, v21
	v_add_f32_dpp v18, v24, v24 row_shr:1 row_mask:0xf bank_mask:0xf bound_ctrl:1
	v_mov_b32_e32 v19, v69
	v_and_b32_e32 v42, 0xffff0000, v21
	v_add_f32_dpp v18, v18, v18 row_shr:2 row_mask:0xf bank_mask:0xf bound_ctrl:1
	s_nop 1
	v_add_f32_dpp v18, v18, v18 row_shr:4 row_mask:0xf bank_mask:0xf bound_ctrl:1
	s_nop 1
	v_add_f32_dpp v18, v18, v18 row_shr:8 row_mask:0xf bank_mask:0xf bound_ctrl:1
	s_nop 1
	v_mov_b32_dpp v19, v18 row_bcast:15 row_mask:0xa bank_mask:0xf bound_ctrl:1
	v_add_f32_e32 v18, v18, v19
	v_mov_b32_e32 v19, v69
	s_nop 1
	v_mov_b32_dpp v19, v18 row_bcast:31 row_mask:0xc bank_mask:0xf bound_ctrl:1
	v_add_f32_e32 v18, v18, v19
	v_mov_b32_e32 v19, v69
	v_readlane_b32 s14, v18, 63
	s_nop 1
	v_sub_f32_e32 v18, s14, v18
	v_add_f32_e32 v22, v18, v24
	v_sub_f32_e32 v22, s14, v22
	v_add_f32_dpp v18, v25, v25 row_shr:1 row_mask:0xf bank_mask:0xf bound_ctrl:1
	v_mul_f32_e32 v22, 0x3fb8aa3b, v22
	v_exp_f32_e32 v22, v22
	v_add_f32_dpp v18, v18, v18 row_shr:2 row_mask:0xf bank_mask:0xf bound_ctrl:1
	s_nop 1
	v_add_f32_dpp v18, v18, v18 row_shr:4 row_mask:0xf bank_mask:0xf bound_ctrl:1
	s_nop 1
	v_add_f32_dpp v18, v18, v18 row_shr:8 row_mask:0xf bank_mask:0xf bound_ctrl:1
	s_nop 1
	v_mov_b32_dpp v19, v18 row_bcast:15 row_mask:0xa bank_mask:0xf bound_ctrl:1
	v_add_f32_e32 v18, v18, v19
	v_mov_b32_e32 v19, v69
	s_nop 1
	v_mov_b32_dpp v19, v18 row_bcast:31 row_mask:0xc bank_mask:0xf bound_ctrl:1
	v_add_f32_e32 v18, v18, v19
	v_mov_b32_e32 v19, v69
	v_readlane_b32 s15, v18, 63
	s_nop 1
	v_sub_f32_e32 v18, s15, v18
	v_add_f32_e32 v23, v18, v25
	s_nop 0
	v_add_f32_dpp v18, v37, v37 row_shr:1 row_mask:0xf bank_mask:0xf bound_ctrl:1
	s_nop 1
	v_add_f32_dpp v18, v18, v18 row_shr:2 row_mask:0xf bank_mask:0xf bound_ctrl:1
	s_nop 1
	v_add_f32_dpp v18, v18, v18 row_shr:4 row_mask:0xf bank_mask:0xf bound_ctrl:1
	s_nop 1
	v_add_f32_dpp v18, v18, v18 row_shr:8 row_mask:0xf bank_mask:0xf bound_ctrl:1
	s_nop 1
	v_mov_b32_dpp v19, v18 row_bcast:15 row_mask:0xa bank_mask:0xf bound_ctrl:1
	v_add_f32_e32 v18, v18, v19
	v_mov_b32_e32 v19, v69
	s_nop 1
	v_mov_b32_dpp v19, v18 row_bcast:31 row_mask:0xc bank_mask:0xf bound_ctrl:1
	v_add_f32_e32 v18, v18, v19
	v_mov_b32_e32 v19, v69
	v_readlane_b32 s26, v18, 63
	s_nop 1
	v_sub_f32_e32 v18, s26, v18
	v_add_f32_e32 v24, v18, v37
	s_nop 0
	v_add_f32_dpp v18, v38, v38 row_shr:1 row_mask:0xf bank_mask:0xf bound_ctrl:1
	s_nop 1
	v_add_f32_dpp v18, v18, v18 row_shr:2 row_mask:0xf bank_mask:0xf bound_ctrl:1
	s_nop 1
	v_add_f32_dpp v18, v18, v18 row_shr:4 row_mask:0xf bank_mask:0xf bound_ctrl:1
	s_nop 1
	v_add_f32_dpp v18, v18, v18 row_shr:8 row_mask:0xf bank_mask:0xf bound_ctrl:1
	s_nop 1
	v_mov_b32_dpp v19, v18 row_bcast:15 row_mask:0xa bank_mask:0xf bound_ctrl:1
	v_add_f32_e32 v18, v18, v19
	v_mov_b32_e32 v19, v69
	s_nop 1
	v_mov_b32_dpp v19, v18 row_bcast:31 row_mask:0xc bank_mask:0xf bound_ctrl:1
	v_add_f32_e32 v18, v18, v19
	v_mov_b32_e32 v19, v69
	v_readlane_b32 s65, v18, 63
	s_nop 1
	v_sub_f32_e32 v18, s65, v18
	v_add_f32_e32 v25, v18, v38
	s_nop 0
	v_add_f32_dpp v18, v39, v39 row_shr:1 row_mask:0xf bank_mask:0xf bound_ctrl:1
	s_nop 1
	v_add_f32_dpp v18, v18, v18 row_shr:2 row_mask:0xf bank_mask:0xf bound_ctrl:1
	s_nop 1
	v_add_f32_dpp v18, v18, v18 row_shr:4 row_mask:0xf bank_mask:0xf bound_ctrl:1
	s_nop 1
	v_add_f32_dpp v18, v18, v18 row_shr:8 row_mask:0xf bank_mask:0xf bound_ctrl:1
	s_nop 1
	v_mov_b32_dpp v19, v18 row_bcast:15 row_mask:0xa bank_mask:0xf bound_ctrl:1
	v_add_f32_e32 v18, v18, v19
	v_mov_b32_e32 v19, v69
	s_nop 1
	v_mov_b32_dpp v19, v18 row_bcast:31 row_mask:0xc bank_mask:0xf bound_ctrl:1
	v_add_f32_e32 v18, v18, v19
	v_mov_b32_e32 v19, v69
	v_readlane_b32 s69, v18, 63
	s_nop 1
	v_sub_f32_e32 v18, s69, v18
	v_add_f32_e32 v37, v18, v39
	s_nop 0
	v_add_f32_dpp v18, v40, v40 row_shr:1 row_mask:0xf bank_mask:0xf bound_ctrl:1
	s_nop 1
	v_add_f32_dpp v18, v18, v18 row_shr:2 row_mask:0xf bank_mask:0xf bound_ctrl:1
	s_nop 1
	v_add_f32_dpp v18, v18, v18 row_shr:4 row_mask:0xf bank_mask:0xf bound_ctrl:1
	s_nop 1
	v_add_f32_dpp v18, v18, v18 row_shr:8 row_mask:0xf bank_mask:0xf bound_ctrl:1
	s_nop 1
	v_mov_b32_dpp v19, v18 row_bcast:15 row_mask:0xa bank_mask:0xf bound_ctrl:1
	v_add_f32_e32 v18, v18, v19
	v_mov_b32_e32 v19, v69
	s_nop 1
	v_mov_b32_dpp v19, v18 row_bcast:31 row_mask:0xc bank_mask:0xf bound_ctrl:1
	v_add_f32_e32 v18, v18, v19
	v_mov_b32_e32 v19, v69
	v_readlane_b32 s71, v18, 63
	s_nop 1
	v_sub_f32_e32 v18, s71, v18
	v_add_f32_e32 v38, v18, v40
	s_nop 0
	v_add_f32_dpp v18, v41, v41 row_shr:1 row_mask:0xf bank_mask:0xf bound_ctrl:1
	s_nop 1
	v_add_f32_dpp v18, v18, v18 row_shr:2 row_mask:0xf bank_mask:0xf bound_ctrl:1
	s_nop 1
	v_add_f32_dpp v18, v18, v18 row_shr:4 row_mask:0xf bank_mask:0xf bound_ctrl:1
	s_nop 1
	v_add_f32_dpp v18, v18, v18 row_shr:8 row_mask:0xf bank_mask:0xf bound_ctrl:1
	s_nop 1
	v_mov_b32_dpp v19, v18 row_bcast:15 row_mask:0xa bank_mask:0xf bound_ctrl:1
	v_add_f32_e32 v18, v18, v19
	v_mov_b32_e32 v19, v69
	s_nop 1
	v_mov_b32_dpp v19, v18 row_bcast:31 row_mask:0xc bank_mask:0xf bound_ctrl:1
	v_add_f32_e32 v18, v18, v19
	v_mov_b32_e32 v19, v69
	v_readlane_b32 s74, v18, 63
	s_nop 1
	v_sub_f32_e32 v18, s74, v18
	v_add_f32_e32 v39, v18, v41
	s_nop 0
	v_add_f32_dpp v18, v42, v42 row_shr:1 row_mask:0xf bank_mask:0xf bound_ctrl:1
	s_nop 1
	v_add_f32_dpp v18, v18, v18 row_shr:2 row_mask:0xf bank_mask:0xf bound_ctrl:1
	s_nop 1
	v_add_f32_dpp v18, v18, v18 row_shr:4 row_mask:0xf bank_mask:0xf bound_ctrl:1
	s_nop 1
	v_add_f32_dpp v18, v18, v18 row_shr:8 row_mask:0xf bank_mask:0xf bound_ctrl:1
	s_nop 1
	v_mov_b32_dpp v19, v18 row_bcast:15 row_mask:0xa bank_mask:0xf bound_ctrl:1
	v_add_f32_e32 v18, v18, v19
	v_mov_b32_e32 v19, v69
	s_nop 1
	v_mov_b32_dpp v19, v18 row_bcast:31 row_mask:0xc bank_mask:0xf bound_ctrl:1
	v_add_f32_e32 v18, v18, v19
	s_nop 0
	v_readlane_b32 s75, v18, 63
	s_nop 1
	v_sub_f32_e32 v18, s75, v18
	v_add_f32_e32 v40, v18, v42
	ds_read_b128 v[18:21], v58
	s_waitcnt lgkmcnt(0)
	v_lshlrev_b32_e32 v41, 16, v18
	v_mul_f32_e32 v22, v22, v41
	v_cvt_pk_bf16_f32 v22, v22, s0
	ds_write_b16 v59, v22 offset:26624
	v_sub_f32_e32 v22, s48, v87
	v_mul_f32_e32 v22, 0x3fb8aa3b, v22
	v_exp_f32_e32 v22, v22
	v_and_b32_e32 v18, 0xffff0000, v18
	v_lshlrev_b32_e32 v42, 16, v19
	v_and_b32_e32 v19, 0xffff0000, v19
	v_mul_f32_e32 v22, v22, v18
	v_cvt_pk_bf16_f32 v22, v22, s0
	ds_write_b16 v59, v22 offset:17552
	v_sub_f32_e32 v22, s15, v23
	v_mul_f32_e32 v22, 0x3fb8aa3b, v22
	v_exp_f32_e32 v22, v22
	v_lshlrev_b32_e32 v43, 16, v20
	v_and_b32_e32 v20, 0xffff0000, v20
	v_lshlrev_b32_e32 v44, 16, v21
	v_mul_f32_e32 v18, v22, v18
	v_cvt_pk_bf16_f32 v18, v18, s0
	ds_write_b16 v59, v18 offset:26768
	v_sub_f32_e32 v18, s50, v86
	v_mul_f32_e32 v18, 0x3fb8aa3b, v18
	v_exp_f32_e32 v18, v18
	v_and_b32_e32 v21, 0xffff0000, v21
	v_mul_f32_e32 v45, v45, v41
	v_cvt_pk_bf16_f32 v45, v45, s0
	v_mul_f32_e32 v18, v18, v42
	v_cvt_pk_bf16_f32 v18, v18, s0
	ds_write_b16 v59, v18 offset:17696
	v_sub_f32_e32 v18, s26, v24
	v_mul_f32_e32 v18, 0x3fb8aa3b, v18
	v_exp_f32_e32 v18, v18
	ds_write_b16 v59, v45 offset:17408
	v_mul_f32_e32 v18, v18, v42
	v_cvt_pk_bf16_f32 v18, v18, s0
	ds_write_b16 v59, v18 offset:26912
	v_sub_f32_e32 v18, s56, v85
	v_mul_f32_e32 v18, 0x3fb8aa3b, v18
	v_exp_f32_e32 v18, v18
	s_nop 0
	v_mul_f32_e32 v18, v18, v19
	v_cvt_pk_bf16_f32 v18, v18, s0
	ds_write_b16 v59, v18 offset:17840
	v_sub_f32_e32 v18, s65, v25
	v_mul_f32_e32 v18, 0x3fb8aa3b, v18
	v_exp_f32_e32 v18, v18
	s_nop 0
	v_mul_f32_e32 v18, v18, v19
	v_cvt_pk_bf16_f32 v18, v18, s0
	ds_write_b16 v59, v18 offset:27056
	v_sub_f32_e32 v18, s49, v84
	v_mul_f32_e32 v18, 0x3fb8aa3b, v18
	v_exp_f32_e32 v18, v18
	s_nop 0
	v_mul_f32_e32 v18, v18, v43
	v_cvt_pk_bf16_f32 v18, v18, s0
	ds_write_b16 v59, v18 offset:17984
	v_sub_f32_e32 v18, s69, v37
	v_mul_f32_e32 v18, 0x3fb8aa3b, v18
	v_exp_f32_e32 v18, v18
	s_nop 0
	v_mul_f32_e32 v18, v18, v43
	v_cvt_pk_bf16_f32 v18, v18, s0
	ds_write_b16 v59, v18 offset:27200
	v_sub_f32_e32 v18, s51, v83
	v_mul_f32_e32 v18, 0x3fb8aa3b, v18
	v_exp_f32_e32 v18, v18
	s_nop 0
	v_mul_f32_e32 v18, v18, v20
	v_cvt_pk_bf16_f32 v18, v18, s0
	ds_write_b16 v59, v18 offset:18128
	v_sub_f32_e32 v18, s71, v38
	v_mul_f32_e32 v18, 0x3fb8aa3b, v18
	v_exp_f32_e32 v18, v18
	s_nop 0
	v_mul_f32_e32 v18, v18, v20
	v_cvt_pk_bf16_f32 v18, v18, s0
	ds_write_b16 v59, v18 offset:27344
	v_sub_f32_e32 v18, s57, v82
	v_mul_f32_e32 v18, 0x3fb8aa3b, v18
	v_exp_f32_e32 v18, v18
	s_nop 0
	v_mul_f32_e32 v18, v18, v44
	v_cvt_pk_bf16_f32 v18, v18, s0
	ds_write_b16 v59, v18 offset:18272
	v_sub_f32_e32 v18, s74, v39
	v_mul_f32_e32 v18, 0x3fb8aa3b, v18
	v_exp_f32_e32 v18, v18
	s_nop 0
	v_mul_f32_e32 v18, v18, v44
	v_cvt_pk_bf16_f32 v18, v18, s0
	ds_write_b16 v59, v18 offset:27488
	v_sub_f32_e32 v18, s70, v81
	v_mul_f32_e32 v18, 0x3fb8aa3b, v18
	v_exp_f32_e32 v18, v18
	s_nop 0
	v_mul_f32_e32 v18, v18, v21
	v_cvt_pk_bf16_f32 v18, v18, s0
	ds_write_b16 v59, v18 offset:18416
	v_sub_f32_e32 v18, s75, v40
	v_mul_f32_e32 v18, 0x3fb8aa3b, v18
	v_exp_f32_e32 v18, v18
	s_nop 0
	v_mul_f32_e32 v18, v18, v21
	v_cvt_pk_bf16_f32 v18, v18, s0
	ds_write_b16 v59, v18 offset:27632
	s_and_saveexec_b64 s[0:1], s[4:5]
	s_cbranch_execz .LBB0_503
	s_cmp_gt_i32 s44, 3
	s_cselect_b32 s36, 0x87, 3
	s_mul_i32 s64, s45, 0x39c
	s_add_i32 s77, s21, s25
	s_add_i32 s78, s77, s64
	s_mul_i32 s64, s45, 0x4a4
	v_mul_f32_e32 v19, s14, v244
	v_mul_f32_e32 v20, s15, v244
	v_mul_f32_e32 v21, s26, v244
	s_add_i32 s36, s36, s64
	s_add_i32 s64, s21, s39
	v_mul_f32_e32 v18, s27, v244
	v_exp_f32_e32 v22, v19
	v_mul_f32_e32 v19, s48, v244
	v_exp_f32_e32 v23, v20
	v_mul_f32_e32 v20, s50, v244
	v_exp_f32_e32 v24, v21
	v_mul_f32_e32 v21, s56, v244
	s_add_i32 s36, s64, s36
	s_ashr_i32 s79, s78, 31
	v_exp_f32_e32 v18, v18
	v_exp_f32_e32 v19, v19
	v_exp_f32_e32 v20, v20
	v_exp_f32_e32 v21, v21
	s_add_i32 s80, s36, 0x84
	s_lshl_b64 s[78:79], s[78:79], 8
	s_add_u32 s78, s34, s78
	s_addc_u32 s79, s35, s79
	global_store_dwordx4 v69, v[18:21], s[78:79]
	s_ashr_i32 s81, s80, 31
	s_lshl_b64 s[80:81], s[80:81], 8
	v_mul_f32_e32 v18, s65, v244
	v_exp_f32_e32 v25, v18
	s_add_u32 s80, s34, s80
	s_addc_u32 s81, s35, s81
	v_mul_f32_e32 v19, s69, v244
	v_mul_f32_e32 v20, s71, v244
	v_mul_f32_e32 v21, s74, v244
	global_store_dwordx4 v69, v[22:25], s[80:81]
	v_mul_f32_e32 v18, s49, v244
	v_exp_f32_e32 v18, v18
	v_exp_f32_e32 v22, v19
	v_mul_f32_e32 v19, s51, v244
	v_exp_f32_e32 v23, v20
	v_mul_f32_e32 v20, s57, v244
	v_exp_f32_e32 v24, v21
	v_mul_f32_e32 v21, s70, v244
	v_exp_f32_e32 v19, v19
	v_exp_f32_e32 v20, v20
	v_exp_f32_e32 v21, v21
	global_store_dwordx4 v69, v[18:21], s[78:79] offset:16
	s_nop 1
	v_mul_f32_e32 v18, s75, v244
	v_exp_f32_e32 v25, v18
	global_store_dwordx4 v69, v[22:25], s[80:81] offset:16
